# baseline (speedup 1.0000x reference)
.LBB2_132:
	s_load_dwordx8 s[4:11], s[0:1], 0x0
	s_load_dwordx2 s[12:13], s[0:1], 0x20
	s_load_dwordx2 s[34:35], s[0:1], 0x28
	s_lshr_b32 s24, s2, 0
	s_and_b32 s25, s2, 0
	s_mul_i32 s26, s25, 16
	s_add_u32 s27, s26, 16
	v_lshl_or_b32 v55, s24, 14, v0
	s_waitcnt lgkmcnt(0)
	s_mov_b32 s14, 0x61a80
	s_mov_b32 s15, 0xf4240
	s_mov_b32 s16, 0x155cc0
	v_mov_b32_e32 v34, s4
	v_mov_b32_e32 v37, s5
	v_mov_b32_e32 v35, s6
	v_mov_b32_e32 v38, s7
	v_mov_b32_e32 v36, s8
	v_mov_b32_e32 v39, s9
	v_mov_b32_e32 v43, 0
	v_mov_b32_e32 v47, 0
	v_mov_b32_e32 v49, 0x30d40
	v_mov_b32_e32 v50, 0xfff6d840
	v_mov_b32_e32 v48, 0x61a80
	v_mov_b32_e32 v51, 0x61a80
	v_mov_b32_e32 v52, 0xf4240
	v_mov_b32_e32 v53, 0x30d40
	v_mov_b32_e32 v54, 0x61a80
	v_cmp_gt_u32_e64 s[18:19], s14, v55
	v_cmp_gt_u32_e64 s[20:21], s15, v55
	v_cmp_gt_u32_e64 s[22:23], s16, v55
	s_nop 0
	v_cndmask_b32_e64 v44, v36, v35, s[20:21]
	v_cndmask_b32_e64 v44, v44, v34, s[18:19]
	v_cndmask_b32_e64 v45, v39, v38, s[20:21]
	v_cndmask_b32_e64 v45, v45, v37, s[18:19]
	v_cndmask_b32_e64 v42, v50, v49, s[20:21]
	v_cndmask_b32_e64 v42, v42, v48, s[18:19]
	v_add_u32_e32 v42, v42, v55
	v_cndmask_b32_e64 v42, 0, v42, s[22:23]
	v_lshl_add_u64 v[46:47], v[42:43], 2, v[44:45]
	global_load_dword v3, v[46:47], off
	v_cndmask_b32_e64 v42, v52, v51, s[20:21]
	v_cndmask_b32_e64 v42, v42, 0, s[18:19]
	v_sub_u32_e32 v42, v55, v42
	v_cndmask_b32_e64 v42, 0, v42, s[22:23]
	v_lshl_add_u64 v[46:47], v[42:43], 2, v[44:45]
	global_load_dword v2, v[46:47], off
	v_add_u32_e32 v40, 0x400, v55
	v_cmp_gt_u32_e64 s[18:19], s14, v40
	v_cmp_gt_u32_e64 s[20:21], s15, v40
	v_cmp_gt_u32_e64 s[22:23], s16, v40
	s_nop 0
	v_cndmask_b32_e64 v44, v36, v35, s[20:21]
	v_cndmask_b32_e64 v44, v44, v34, s[18:19]
	v_cndmask_b32_e64 v45, v39, v38, s[20:21]
	v_cndmask_b32_e64 v45, v45, v37, s[18:19]
	v_cndmask_b32_e64 v42, v50, v49, s[20:21]
	v_cndmask_b32_e64 v42, v42, v48, s[18:19]
	v_add_u32_e32 v42, v42, v40
	v_cndmask_b32_e64 v42, 0, v42, s[22:23]
	v_lshl_add_u64 v[46:47], v[42:43], 2, v[44:45]
	global_load_dword v5, v[46:47], off
	v_cndmask_b32_e64 v42, v52, v51, s[20:21]
	v_cndmask_b32_e64 v42, v42, 0, s[18:19]
	v_sub_u32_e32 v42, v40, v42
	v_cndmask_b32_e64 v42, 0, v42, s[22:23]
	v_lshl_add_u64 v[46:47], v[42:43], 2, v[44:45]
	global_load_dword v4, v[46:47], off
	v_add_u32_e32 v40, 0x800, v55
	v_cmp_gt_u32_e64 s[18:19], s14, v40
	v_cmp_gt_u32_e64 s[20:21], s15, v40
	v_cmp_gt_u32_e64 s[22:23], s16, v40
	s_nop 0
	v_cndmask_b32_e64 v44, v36, v35, s[20:21]
	v_cndmask_b32_e64 v44, v44, v34, s[18:19]
	v_cndmask_b32_e64 v45, v39, v38, s[20:21]
	v_cndmask_b32_e64 v45, v45, v37, s[18:19]
	v_cndmask_b32_e64 v42, v50, v49, s[20:21]
	v_cndmask_b32_e64 v42, v42, v48, s[18:19]
	v_add_u32_e32 v42, v42, v40
	v_cndmask_b32_e64 v42, 0, v42, s[22:23]
	v_lshl_add_u64 v[46:47], v[42:43], 2, v[44:45]
	global_load_dword v7, v[46:47], off
	v_cndmask_b32_e64 v42, v52, v51, s[20:21]
	v_cndmask_b32_e64 v42, v42, 0, s[18:19]
	v_sub_u32_e32 v42, v40, v42
	v_cndmask_b32_e64 v42, 0, v42, s[22:23]
	v_lshl_add_u64 v[46:47], v[42:43], 2, v[44:45]
	global_load_dword v6, v[46:47], off
	v_add_u32_e32 v40, 0xc00, v55
	v_cmp_gt_u32_e64 s[18:19], s14, v40
	v_cmp_gt_u32_e64 s[20:21], s15, v40
	v_cmp_gt_u32_e64 s[22:23], s16, v40
	s_nop 0
	v_cndmask_b32_e64 v44, v36, v35, s[20:21]
	v_cndmask_b32_e64 v44, v44, v34, s[18:19]
	v_cndmask_b32_e64 v45, v39, v38, s[20:21]
	v_cndmask_b32_e64 v45, v45, v37, s[18:19]
	v_cndmask_b32_e64 v42, v50, v49, s[20:21]
	v_cndmask_b32_e64 v42, v42, v48, s[18:19]
	v_add_u32_e32 v42, v42, v40
	v_cndmask_b32_e64 v42, 0, v42, s[22:23]
	v_lshl_add_u64 v[46:47], v[42:43], 2, v[44:45]
	global_load_dword v9, v[46:47], off
	v_cndmask_b32_e64 v42, v52, v51, s[20:21]
	v_cndmask_b32_e64 v42, v42, 0, s[18:19]
	v_sub_u32_e32 v42, v40, v42
	v_cndmask_b32_e64 v42, 0, v42, s[22:23]
	v_lshl_add_u64 v[46:47], v[42:43], 2, v[44:45]
	global_load_dword v8, v[46:47], off
	v_add_u32_e32 v40, 0x1000, v55
	v_cmp_gt_u32_e64 s[18:19], s14, v40
	v_cmp_gt_u32_e64 s[20:21], s15, v40
	v_cmp_gt_u32_e64 s[22:23], s16, v40
	s_nop 0
	v_cndmask_b32_e64 v44, v36, v35, s[20:21]
	v_cndmask_b32_e64 v44, v44, v34, s[18:19]
	v_cndmask_b32_e64 v45, v39, v38, s[20:21]
	v_cndmask_b32_e64 v45, v45, v37, s[18:19]
	v_cndmask_b32_e64 v42, v50, v49, s[20:21]
	v_cndmask_b32_e64 v42, v42, v48, s[18:19]
	v_add_u32_e32 v42, v42, v40
	v_cndmask_b32_e64 v42, 0, v42, s[22:23]
	v_lshl_add_u64 v[46:47], v[42:43], 2, v[44:45]
	global_load_dword v11, v[46:47], off
	v_cndmask_b32_e64 v42, v52, v51, s[20:21]
	v_cndmask_b32_e64 v42, v42, 0, s[18:19]
	v_sub_u32_e32 v42, v40, v42
	v_cndmask_b32_e64 v42, 0, v42, s[22:23]
	v_lshl_add_u64 v[46:47], v[42:43], 2, v[44:45]
	global_load_dword v10, v[46:47], off
	v_add_u32_e32 v40, 0x1400, v55
	v_cmp_gt_u32_e64 s[18:19], s14, v40
	v_cmp_gt_u32_e64 s[20:21], s15, v40
	v_cmp_gt_u32_e64 s[22:23], s16, v40
	s_nop 0
	v_cndmask_b32_e64 v44, v36, v35, s[20:21]
	v_cndmask_b32_e64 v44, v44, v34, s[18:19]
	v_cndmask_b32_e64 v45, v39, v38, s[20:21]
	v_cndmask_b32_e64 v45, v45, v37, s[18:19]
	v_cndmask_b32_e64 v42, v50, v49, s[20:21]
	v_cndmask_b32_e64 v42, v42, v48, s[18:19]
	v_add_u32_e32 v42, v42, v40
	v_cndmask_b32_e64 v42, 0, v42, s[22:23]
	v_lshl_add_u64 v[46:47], v[42:43], 2, v[44:45]
	global_load_dword v13, v[46:47], off
	v_cndmask_b32_e64 v42, v52, v51, s[20:21]
	v_cndmask_b32_e64 v42, v42, 0, s[18:19]
	v_sub_u32_e32 v42, v40, v42
	v_cndmask_b32_e64 v42, 0, v42, s[22:23]
	v_lshl_add_u64 v[46:47], v[42:43], 2, v[44:45]
	global_load_dword v12, v[46:47], off
	v_add_u32_e32 v40, 0x1800, v55
	v_cmp_gt_u32_e64 s[18:19], s14, v40
	v_cmp_gt_u32_e64 s[20:21], s15, v40
	v_cmp_gt_u32_e64 s[22:23], s16, v40
	s_nop 0
	v_cndmask_b32_e64 v44, v36, v35, s[20:21]
	v_cndmask_b32_e64 v44, v44, v34, s[18:19]
	v_cndmask_b32_e64 v45, v39, v38, s[20:21]
	v_cndmask_b32_e64 v45, v45, v37, s[18:19]
	v_cndmask_b32_e64 v42, v50, v49, s[20:21]
	v_cndmask_b32_e64 v42, v42, v48, s[18:19]
	v_add_u32_e32 v42, v42, v40
	v_cndmask_b32_e64 v42, 0, v42, s[22:23]
	v_lshl_add_u64 v[46:47], v[42:43], 2, v[44:45]
	global_load_dword v15, v[46:47], off
	v_cndmask_b32_e64 v42, v52, v51, s[20:21]
	v_cndmask_b32_e64 v42, v42, 0, s[18:19]
	v_sub_u32_e32 v42, v40, v42
	v_cndmask_b32_e64 v42, 0, v42, s[22:23]
	v_lshl_add_u64 v[46:47], v[42:43], 2, v[44:45]
	global_load_dword v14, v[46:47], off
	v_add_u32_e32 v40, 0x1c00, v55
	v_cmp_gt_u32_e64 s[18:19], s14, v40
	v_cmp_gt_u32_e64 s[20:21], s15, v40
	v_cmp_gt_u32_e64 s[22:23], s16, v40
	s_nop 0
	v_cndmask_b32_e64 v44, v36, v35, s[20:21]
	v_cndmask_b32_e64 v44, v44, v34, s[18:19]
	v_cndmask_b32_e64 v45, v39, v38, s[20:21]
	v_cndmask_b32_e64 v45, v45, v37, s[18:19]
	v_cndmask_b32_e64 v42, v50, v49, s[20:21]
	v_cndmask_b32_e64 v42, v42, v48, s[18:19]
	v_add_u32_e32 v42, v42, v40
	v_cndmask_b32_e64 v42, 0, v42, s[22:23]
	v_lshl_add_u64 v[46:47], v[42:43], 2, v[44:45]
	global_load_dword v17, v[46:47], off
	v_cndmask_b32_e64 v42, v52, v51, s[20:21]
	v_cndmask_b32_e64 v42, v42, 0, s[18:19]
	v_sub_u32_e32 v42, v40, v42
	v_cndmask_b32_e64 v42, 0, v42, s[22:23]
	v_lshl_add_u64 v[46:47], v[42:43], 2, v[44:45]
	global_load_dword v16, v[46:47], off
	v_add_u32_e32 v40, 0x2000, v55
	v_cmp_gt_u32_e64 s[18:19], s14, v40
	v_cmp_gt_u32_e64 s[20:21], s15, v40
	v_cmp_gt_u32_e64 s[22:23], s16, v40
	s_nop 0
	v_cndmask_b32_e64 v44, v36, v35, s[20:21]
	v_cndmask_b32_e64 v44, v44, v34, s[18:19]
	v_cndmask_b32_e64 v45, v39, v38, s[20:21]
	v_cndmask_b32_e64 v45, v45, v37, s[18:19]
	v_cndmask_b32_e64 v42, v50, v49, s[20:21]
	v_cndmask_b32_e64 v42, v42, v48, s[18:19]
	v_add_u32_e32 v42, v42, v40
	v_cndmask_b32_e64 v42, 0, v42, s[22:23]
	v_lshl_add_u64 v[46:47], v[42:43], 2, v[44:45]
	global_load_dword v19, v[46:47], off
	v_cndmask_b32_e64 v42, v52, v51, s[20:21]
	v_cndmask_b32_e64 v42, v42, 0, s[18:19]
	v_sub_u32_e32 v42, v40, v42
	v_cndmask_b32_e64 v42, 0, v42, s[22:23]
	v_lshl_add_u64 v[46:47], v[42:43], 2, v[44:45]
	global_load_dword v18, v[46:47], off
	v_add_u32_e32 v40, 0x2400, v55
	v_cmp_gt_u32_e64 s[18:19], s14, v40
	v_cmp_gt_u32_e64 s[20:21], s15, v40
	v_cmp_gt_u32_e64 s[22:23], s16, v40
	s_nop 0
	v_cndmask_b32_e64 v44, v36, v35, s[20:21]
	v_cndmask_b32_e64 v44, v44, v34, s[18:19]
	v_cndmask_b32_e64 v45, v39, v38, s[20:21]
	v_cndmask_b32_e64 v45, v45, v37, s[18:19]
	v_cndmask_b32_e64 v42, v50, v49, s[20:21]
	v_cndmask_b32_e64 v42, v42, v48, s[18:19]
	v_add_u32_e32 v42, v42, v40
	v_cndmask_b32_e64 v42, 0, v42, s[22:23]
	v_lshl_add_u64 v[46:47], v[42:43], 2, v[44:45]
	global_load_dword v21, v[46:47], off
	v_cndmask_b32_e64 v42, v52, v51, s[20:21]
	v_cndmask_b32_e64 v42, v42, 0, s[18:19]
	v_sub_u32_e32 v42, v40, v42
	v_cndmask_b32_e64 v42, 0, v42, s[22:23]
	v_lshl_add_u64 v[46:47], v[42:43], 2, v[44:45]
	global_load_dword v20, v[46:47], off
	v_add_u32_e32 v40, 0x2800, v55
	v_cmp_gt_u32_e64 s[18:19], s14, v40
	v_cmp_gt_u32_e64 s[20:21], s15, v40
	v_cmp_gt_u32_e64 s[22:23], s16, v40
	s_nop 0
	v_cndmask_b32_e64 v44, v36, v35, s[20:21]
	v_cndmask_b32_e64 v44, v44, v34, s[18:19]
	v_cndmask_b32_e64 v45, v39, v38, s[20:21]
	v_cndmask_b32_e64 v45, v45, v37, s[18:19]
	v_cndmask_b32_e64 v42, v50, v49, s[20:21]
	v_cndmask_b32_e64 v42, v42, v48, s[18:19]
	v_add_u32_e32 v42, v42, v40
	v_cndmask_b32_e64 v42, 0, v42, s[22:23]
	v_lshl_add_u64 v[46:47], v[42:43], 2, v[44:45]
	global_load_dword v23, v[46:47], off
	v_cndmask_b32_e64 v42, v52, v51, s[20:21]
	v_cndmask_b32_e64 v42, v42, 0, s[18:19]
	v_sub_u32_e32 v42, v40, v42
	v_cndmask_b32_e64 v42, 0, v42, s[22:23]
	v_lshl_add_u64 v[46:47], v[42:43], 2, v[44:45]
	global_load_dword v22, v[46:47], off
	v_add_u32_e32 v40, 0x2c00, v55
	v_cmp_gt_u32_e64 s[18:19], s14, v40
	v_cmp_gt_u32_e64 s[20:21], s15, v40
	v_cmp_gt_u32_e64 s[22:23], s16, v40
	s_nop 0
	v_cndmask_b32_e64 v44, v36, v35, s[20:21]
	v_cndmask_b32_e64 v44, v44, v34, s[18:19]
	v_cndmask_b32_e64 v45, v39, v38, s[20:21]
	v_cndmask_b32_e64 v45, v45, v37, s[18:19]
	v_cndmask_b32_e64 v42, v50, v49, s[20:21]
	v_cndmask_b32_e64 v42, v42, v48, s[18:19]
	v_add_u32_e32 v42, v42, v40
	v_cndmask_b32_e64 v42, 0, v42, s[22:23]
	v_lshl_add_u64 v[46:47], v[42:43], 2, v[44:45]
	global_load_dword v25, v[46:47], off
	v_cndmask_b32_e64 v42, v52, v51, s[20:21]
	v_cndmask_b32_e64 v42, v42, 0, s[18:19]
	v_sub_u32_e32 v42, v40, v42
	v_cndmask_b32_e64 v42, 0, v42, s[22:23]
	v_lshl_add_u64 v[46:47], v[42:43], 2, v[44:45]
	global_load_dword v24, v[46:47], off
	v_add_u32_e32 v40, 0x3000, v55
	v_cmp_gt_u32_e64 s[18:19], s14, v40
	v_cmp_gt_u32_e64 s[20:21], s15, v40
	v_cmp_gt_u32_e64 s[22:23], s16, v40
	s_nop 0
	v_cndmask_b32_e64 v44, v36, v35, s[20:21]
	v_cndmask_b32_e64 v44, v44, v34, s[18:19]
	v_cndmask_b32_e64 v45, v39, v38, s[20:21]
	v_cndmask_b32_e64 v45, v45, v37, s[18:19]
	v_cndmask_b32_e64 v42, v50, v49, s[20:21]
	v_cndmask_b32_e64 v42, v42, v48, s[18:19]
	v_add_u32_e32 v42, v42, v40
	v_cndmask_b32_e64 v42, 0, v42, s[22:23]
	v_lshl_add_u64 v[46:47], v[42:43], 2, v[44:45]
	global_load_dword v27, v[46:47], off
	v_cndmask_b32_e64 v42, v52, v51, s[20:21]
	v_cndmask_b32_e64 v42, v42, 0, s[18:19]
	v_sub_u32_e32 v42, v40, v42
	v_cndmask_b32_e64 v42, 0, v42, s[22:23]
	v_lshl_add_u64 v[46:47], v[42:43], 2, v[44:45]
	global_load_dword v26, v[46:47], off
	v_add_u32_e32 v40, 0x3400, v55
	v_cmp_gt_u32_e64 s[18:19], s14, v40
	v_cmp_gt_u32_e64 s[20:21], s15, v40
	v_cmp_gt_u32_e64 s[22:23], s16, v40
	s_nop 0
	v_cndmask_b32_e64 v44, v36, v35, s[20:21]
	v_cndmask_b32_e64 v44, v44, v34, s[18:19]
	v_cndmask_b32_e64 v45, v39, v38, s[20:21]
	v_cndmask_b32_e64 v45, v45, v37, s[18:19]
	v_cndmask_b32_e64 v42, v50, v49, s[20:21]
	v_cndmask_b32_e64 v42, v42, v48, s[18:19]
	v_add_u32_e32 v42, v42, v40
	v_cndmask_b32_e64 v42, 0, v42, s[22:23]
	v_lshl_add_u64 v[46:47], v[42:43], 2, v[44:45]
	global_load_dword v29, v[46:47], off
	v_cndmask_b32_e64 v42, v52, v51, s[20:21]
	v_cndmask_b32_e64 v42, v42, 0, s[18:19]
	v_sub_u32_e32 v42, v40, v42
	v_cndmask_b32_e64 v42, 0, v42, s[22:23]
	v_lshl_add_u64 v[46:47], v[42:43], 2, v[44:45]
	global_load_dword v28, v[46:47], off
	v_add_u32_e32 v40, 0x3800, v55
	v_cmp_gt_u32_e64 s[18:19], s14, v40
	v_cmp_gt_u32_e64 s[20:21], s15, v40
	v_cmp_gt_u32_e64 s[22:23], s16, v40
	s_nop 0
	v_cndmask_b32_e64 v44, v36, v35, s[20:21]
	v_cndmask_b32_e64 v44, v44, v34, s[18:19]
	v_cndmask_b32_e64 v45, v39, v38, s[20:21]
	v_cndmask_b32_e64 v45, v45, v37, s[18:19]
	v_cndmask_b32_e64 v42, v50, v49, s[20:21]
	v_cndmask_b32_e64 v42, v42, v48, s[18:19]
	v_add_u32_e32 v42, v42, v40
	v_cndmask_b32_e64 v42, 0, v42, s[22:23]
	v_lshl_add_u64 v[46:47], v[42:43], 2, v[44:45]
	global_load_dword v31, v[46:47], off
	v_cndmask_b32_e64 v42, v52, v51, s[20:21]
	v_cndmask_b32_e64 v42, v42, 0, s[18:19]
	v_sub_u32_e32 v42, v40, v42
	v_cndmask_b32_e64 v42, 0, v42, s[22:23]
	v_lshl_add_u64 v[46:47], v[42:43], 2, v[44:45]
	global_load_dword v30, v[46:47], off
	v_add_u32_e32 v40, 0x3c00, v55
	v_cmp_gt_u32_e64 s[18:19], s14, v40
	v_cmp_gt_u32_e64 s[20:21], s15, v40
	v_cmp_gt_u32_e64 s[22:23], s16, v40
	s_nop 0
	v_cndmask_b32_e64 v44, v36, v35, s[20:21]
	v_cndmask_b32_e64 v44, v44, v34, s[18:19]
	v_cndmask_b32_e64 v45, v39, v38, s[20:21]
	v_cndmask_b32_e64 v45, v45, v37, s[18:19]
	v_cndmask_b32_e64 v42, v50, v49, s[20:21]
	v_cndmask_b32_e64 v42, v42, v48, s[18:19]
	v_add_u32_e32 v42, v42, v40
	v_cndmask_b32_e64 v42, 0, v42, s[22:23]
	v_lshl_add_u64 v[46:47], v[42:43], 2, v[44:45]
	global_load_dword v33, v[46:47], off
	v_cndmask_b32_e64 v42, v52, v51, s[20:21]
	v_cndmask_b32_e64 v42, v42, 0, s[18:19]
	v_sub_u32_e32 v42, v40, v42
	v_cndmask_b32_e64 v42, 0, v42, s[22:23]
	v_lshl_add_u64 v[46:47], v[42:43], 2, v[44:45]
	global_load_dword v32, v[46:47], off
	v_mov_b32_e32 v34, 0
	v_mov_b32_e32 v35, 0
	v_mov_b32_e32 v36, 0
	v_mov_b32_e32 v37, 0
	v_lshlrev_b32_e32 v38, 3, v0
	v_cmp_gt_u32_e32 vcc, 0x224, v0
	s_and_saveexec_b64 s[36:37], vcc
	s_cbranch_execz .Lsc_nohist
	global_load_dwordx2 v[40:41], v38, s[10:11]
	v_add_u32_e32 v39, 0x1120, v38
	global_load_dwordx2 v[42:43], v39, s[10:11]
	v_add_u32_e32 v39, 0x2240, v38
	global_load_dwordx2 v[44:45], v39, s[10:11]
	v_add_u32_e32 v39, 0x3360, v38
	global_load_dwordx2 v[46:47], v39, s[10:11]
	v_add_u32_e32 v39, 0x4480, v38
	global_load_dwordx2 v[48:49], v39, s[10:11]
	v_add_u32_e32 v39, 0x55a0, v38
	global_load_dwordx2 v[50:51], v39, s[10:11]
	v_add_u32_e32 v39, 0x66c0, v38
	global_load_dwordx2 v[52:53], v39, s[10:11]
	v_add_u32_e32 v39, 0x77e0, v38
	global_load_dwordx2 v[54:55], v39, s[10:11]
	v_add_u32_e32 v39, 0x8900, v38
	global_load_dwordx2 v[56:57], v39, s[10:11]
	v_add_u32_e32 v39, 0x9a20, v38
	global_load_dwordx2 v[58:59], v39, s[10:11]
	v_add_u32_e32 v39, 0xab40, v38
	global_load_dwordx2 v[60:61], v39, s[10:11]
	v_add_u32_e32 v39, 0xbc60, v38
	global_load_dwordx2 v[62:63], v39, s[10:11]
	v_add_u32_e32 v39, 0xcd80, v38
	global_load_dwordx2 v[64:65], v39, s[10:11]
	v_add_u32_e32 v39, 0xdea0, v38
	global_load_dwordx2 v[66:67], v39, s[10:11]
	v_add_u32_e32 v39, 0xefc0, v38
	global_load_dwordx2 v[68:69], v39, s[10:11]
	v_add_u32_e32 v39, 0x100e0, v38
	global_load_dwordx2 v[70:71], v39, s[10:11]
	v_add_u32_e32 v39, 0x11200, v38
	global_load_dwordx2 v[72:73], v39, s[10:11]
	v_add_u32_e32 v39, 0x12320, v38
	global_load_dwordx2 v[74:75], v39, s[10:11]
	v_add_u32_e32 v39, 0x13440, v38
	global_load_dwordx2 v[76:77], v39, s[10:11]
	v_add_u32_e32 v39, 0x14560, v38
	global_load_dwordx2 v[78:79], v39, s[10:11]
	v_add_u32_e32 v39, 0x15680, v38
	global_load_dwordx2 v[80:81], v39, s[10:11]
	v_add_u32_e32 v39, 0x167a0, v38
	global_load_dwordx2 v[82:83], v39, s[10:11]
	v_add_u32_e32 v39, 0x178c0, v38
	global_load_dwordx2 v[84:85], v39, s[10:11]
	v_add_u32_e32 v39, 0x189e0, v38
	global_load_dwordx2 v[86:87], v39, s[10:11]
	v_add_u32_e32 v39, 0x19b00, v38
	global_load_dwordx2 v[88:89], v39, s[10:11]
	v_add_u32_e32 v39, 0x1ac20, v38
	global_load_dwordx2 v[90:91], v39, s[10:11]
	v_add_u32_e32 v39, 0x1bd40, v38
	global_load_dwordx2 v[92:93], v39, s[10:11]
	v_add_u32_e32 v39, 0x1ce60, v38
	global_load_dwordx2 v[94:95], v39, s[10:11]
	v_add_u32_e32 v39, 0x1df80, v38
	global_load_dwordx2 v[96:97], v39, s[10:11]
	v_add_u32_e32 v39, 0x1f0a0, v38
	global_load_dwordx2 v[98:99], v39, s[10:11]
	v_add_u32_e32 v39, 0x201c0, v38
	global_load_dwordx2 v[100:101], v39, s[10:11]
	v_add_u32_e32 v39, 0x212e0, v38
	global_load_dwordx2 v[102:103], v39, s[10:11]
	v_add_u32_e32 v39, 0x22400, v38
	global_load_dwordx2 v[104:105], v39, s[10:11]
	v_add_u32_e32 v39, 0x23520, v38
	global_load_dwordx2 v[106:107], v39, s[10:11]
	v_add_u32_e32 v39, 0x24640, v38
	global_load_dwordx2 v[108:109], v39, s[10:11]
	v_add_u32_e32 v39, 0x25760, v38
	global_load_dwordx2 v[110:111], v39, s[10:11]
	v_add_u32_e32 v39, 0x26880, v38
	global_load_dwordx2 v[112:113], v39, s[10:11]
	v_add_u32_e32 v39, 0x279a0, v38
	global_load_dwordx2 v[114:115], v39, s[10:11]
	v_add_u32_e32 v39, 0x28ac0, v38
	global_load_dwordx2 v[116:117], v39, s[10:11]
	v_add_u32_e32 v39, 0x29be0, v38
	global_load_dwordx2 v[118:119], v39, s[10:11]
	v_add_u32_e32 v39, 0x2ad00, v38
	global_load_dwordx2 v[120:121], v39, s[10:11]
	v_add_u32_e32 v39, 0x2be20, v38
	global_load_dwordx2 v[122:123], v39, s[10:11]
	v_add_u32_e32 v39, 0x2cf40, v38
	global_load_dwordx2 v[124:125], v39, s[10:11]
	s_waitcnt vmcnt(42)
	s_cmp_gt_u32 s24, 0
	s_cselect_b32 s3, 1, 0
	v_add_u32_e32 v34, v34, v40
	v_add_u32_e32 v35, v35, v41
	v_mad_u32_u24 v36, v40, s3, v36
	v_mad_u32_u24 v37, v41, s3, v37
	v_add_u32_e32 v39, 0x2e060, v38
	global_load_dwordx2 v[40:41], v39, s[10:11]
	s_waitcnt vmcnt(42)
	s_cmp_gt_u32 s24, 1
	s_cselect_b32 s3, 1, 0
	v_add_u32_e32 v34, v34, v42
	v_add_u32_e32 v35, v35, v43
	v_mad_u32_u24 v36, v42, s3, v36
	v_mad_u32_u24 v37, v43, s3, v37
	v_add_u32_e32 v39, 0x2f180, v38
	global_load_dwordx2 v[42:43], v39, s[10:11]
	s_waitcnt vmcnt(42)
	s_cmp_gt_u32 s24, 2
	s_cselect_b32 s3, 1, 0
	v_add_u32_e32 v34, v34, v44
	v_add_u32_e32 v35, v35, v45
	v_mad_u32_u24 v36, v44, s3, v36
	v_mad_u32_u24 v37, v45, s3, v37
	v_add_u32_e32 v39, 0x302a0, v38
	global_load_dwordx2 v[44:45], v39, s[10:11]
	s_waitcnt vmcnt(42)
	s_cmp_gt_u32 s24, 3
	s_cselect_b32 s3, 1, 0
	v_add_u32_e32 v34, v34, v46
	v_add_u32_e32 v35, v35, v47
	v_mad_u32_u24 v36, v46, s3, v36
	v_mad_u32_u24 v37, v47, s3, v37
	v_add_u32_e32 v39, 0x313c0, v38
	global_load_dwordx2 v[46:47], v39, s[10:11]
	s_waitcnt vmcnt(42)
	s_cmp_gt_u32 s24, 4
	s_cselect_b32 s3, 1, 0
	v_add_u32_e32 v34, v34, v48
	v_add_u32_e32 v35, v35, v49
	v_mad_u32_u24 v36, v48, s3, v36
	v_mad_u32_u24 v37, v49, s3, v37
	v_add_u32_e32 v39, 0x324e0, v38
	global_load_dwordx2 v[48:49], v39, s[10:11]
	s_waitcnt vmcnt(42)
	s_cmp_gt_u32 s24, 5
	s_cselect_b32 s3, 1, 0
	v_add_u32_e32 v34, v34, v50
	v_add_u32_e32 v35, v35, v51
	v_mad_u32_u24 v36, v50, s3, v36
	v_mad_u32_u24 v37, v51, s3, v37
	v_add_u32_e32 v39, 0x33600, v38
	global_load_dwordx2 v[50:51], v39, s[10:11]
	s_waitcnt vmcnt(42)
	s_cmp_gt_u32 s24, 6
	s_cselect_b32 s3, 1, 0
	v_add_u32_e32 v34, v34, v52
	v_add_u32_e32 v35, v35, v53
	v_mad_u32_u24 v36, v52, s3, v36
	v_mad_u32_u24 v37, v53, s3, v37
	v_add_u32_e32 v39, 0x34720, v38
	global_load_dwordx2 v[52:53], v39, s[10:11]
	s_waitcnt vmcnt(42)
	s_cmp_gt_u32 s24, 7
	s_cselect_b32 s3, 1, 0
	v_add_u32_e32 v34, v34, v54
	v_add_u32_e32 v35, v35, v55
	v_mad_u32_u24 v36, v54, s3, v36
	v_mad_u32_u24 v37, v55, s3, v37
	v_add_u32_e32 v39, 0x35840, v38
	global_load_dwordx2 v[54:55], v39, s[10:11]
	s_waitcnt vmcnt(42)
	s_cmp_gt_u32 s24, 8
	s_cselect_b32 s3, 1, 0
	v_add_u32_e32 v34, v34, v56
	v_add_u32_e32 v35, v35, v57
	v_mad_u32_u24 v36, v56, s3, v36
	v_mad_u32_u24 v37, v57, s3, v37
	v_add_u32_e32 v39, 0x36960, v38
	global_load_dwordx2 v[56:57], v39, s[10:11]
	s_waitcnt vmcnt(42)
	s_cmp_gt_u32 s24, 9
	s_cselect_b32 s3, 1, 0
	v_add_u32_e32 v34, v34, v58
	v_add_u32_e32 v35, v35, v59
	v_mad_u32_u24 v36, v58, s3, v36
	v_mad_u32_u24 v37, v59, s3, v37
	v_add_u32_e32 v39, 0x37a80, v38
	global_load_dwordx2 v[58:59], v39, s[10:11]
	s_waitcnt vmcnt(42)
	s_cmp_gt_u32 s24, 10
	s_cselect_b32 s3, 1, 0
	v_add_u32_e32 v34, v34, v60
	v_add_u32_e32 v35, v35, v61
	v_mad_u32_u24 v36, v60, s3, v36
	v_mad_u32_u24 v37, v61, s3, v37
	v_add_u32_e32 v39, 0x38ba0, v38
	global_load_dwordx2 v[60:61], v39, s[10:11]
	s_waitcnt vmcnt(42)
	s_cmp_gt_u32 s24, 11
	s_cselect_b32 s3, 1, 0
	v_add_u32_e32 v34, v34, v62
	v_add_u32_e32 v35, v35, v63
	v_mad_u32_u24 v36, v62, s3, v36
	v_mad_u32_u24 v37, v63, s3, v37
	v_add_u32_e32 v39, 0x39cc0, v38
	global_load_dwordx2 v[62:63], v39, s[10:11]
	s_waitcnt vmcnt(42)
	s_cmp_gt_u32 s24, 12
	s_cselect_b32 s3, 1, 0
	v_add_u32_e32 v34, v34, v64
	v_add_u32_e32 v35, v35, v65
	v_mad_u32_u24 v36, v64, s3, v36
	v_mad_u32_u24 v37, v65, s3, v37
	v_add_u32_e32 v39, 0x3ade0, v38
	global_load_dwordx2 v[64:65], v39, s[10:11]
	s_waitcnt vmcnt(42)
	s_cmp_gt_u32 s24, 13
	s_cselect_b32 s3, 1, 0
	v_add_u32_e32 v34, v34, v66
	v_add_u32_e32 v35, v35, v67
	v_mad_u32_u24 v36, v66, s3, v36
	v_mad_u32_u24 v37, v67, s3, v37
	v_add_u32_e32 v39, 0x3bf00, v38
	global_load_dwordx2 v[66:67], v39, s[10:11]
	s_waitcnt vmcnt(42)
	s_cmp_gt_u32 s24, 14
	s_cselect_b32 s3, 1, 0
	v_add_u32_e32 v34, v34, v68
	v_add_u32_e32 v35, v35, v69
	v_mad_u32_u24 v36, v68, s3, v36
	v_mad_u32_u24 v37, v69, s3, v37
	v_add_u32_e32 v39, 0x3d020, v38
	global_load_dwordx2 v[68:69], v39, s[10:11]
	s_waitcnt vmcnt(42)
	s_cmp_gt_u32 s24, 15
	s_cselect_b32 s3, 1, 0
	v_add_u32_e32 v34, v34, v70
	v_add_u32_e32 v35, v35, v71
	v_mad_u32_u24 v36, v70, s3, v36
	v_mad_u32_u24 v37, v71, s3, v37
	v_add_u32_e32 v39, 0x3e140, v38
	global_load_dwordx2 v[70:71], v39, s[10:11]
	s_waitcnt vmcnt(42)
	s_cmp_gt_u32 s24, 16
	s_cselect_b32 s3, 1, 0
	v_add_u32_e32 v34, v34, v72
	v_add_u32_e32 v35, v35, v73
	v_mad_u32_u24 v36, v72, s3, v36
	v_mad_u32_u24 v37, v73, s3, v37
	v_add_u32_e32 v39, 0x3f260, v38
	global_load_dwordx2 v[72:73], v39, s[10:11]
	s_waitcnt vmcnt(42)
	s_cmp_gt_u32 s24, 17
	s_cselect_b32 s3, 1, 0
	v_add_u32_e32 v34, v34, v74
	v_add_u32_e32 v35, v35, v75
	v_mad_u32_u24 v36, v74, s3, v36
	v_mad_u32_u24 v37, v75, s3, v37
	v_add_u32_e32 v39, 0x40380, v38
	global_load_dwordx2 v[74:75], v39, s[10:11]
	s_waitcnt vmcnt(42)
	s_cmp_gt_u32 s24, 18
	s_cselect_b32 s3, 1, 0
	v_add_u32_e32 v34, v34, v76
	v_add_u32_e32 v35, v35, v77
	v_mad_u32_u24 v36, v76, s3, v36
	v_mad_u32_u24 v37, v77, s3, v37
	v_add_u32_e32 v39, 0x414a0, v38
	global_load_dwordx2 v[76:77], v39, s[10:11]
	s_waitcnt vmcnt(42)
	s_cmp_gt_u32 s24, 19
	s_cselect_b32 s3, 1, 0
	v_add_u32_e32 v34, v34, v78
	v_add_u32_e32 v35, v35, v79
	v_mad_u32_u24 v36, v78, s3, v36
	v_mad_u32_u24 v37, v79, s3, v37
	v_add_u32_e32 v39, 0x425c0, v38
	global_load_dwordx2 v[78:79], v39, s[10:11]
	s_waitcnt vmcnt(42)
	s_cmp_gt_u32 s24, 20
	s_cselect_b32 s3, 1, 0
	v_add_u32_e32 v34, v34, v80
	v_add_u32_e32 v35, v35, v81
	v_mad_u32_u24 v36, v80, s3, v36
	v_mad_u32_u24 v37, v81, s3, v37
	v_add_u32_e32 v39, 0x436e0, v38
	global_load_dwordx2 v[80:81], v39, s[10:11]
	s_waitcnt vmcnt(42)
	s_cmp_gt_u32 s24, 21
	s_cselect_b32 s3, 1, 0
	v_add_u32_e32 v34, v34, v82
	v_add_u32_e32 v35, v35, v83
	v_mad_u32_u24 v36, v82, s3, v36
	v_mad_u32_u24 v37, v83, s3, v37
	v_add_u32_e32 v39, 0x44800, v38
	global_load_dwordx2 v[82:83], v39, s[10:11]
	s_waitcnt vmcnt(42)
	s_cmp_gt_u32 s24, 22
	s_cselect_b32 s3, 1, 0
	v_add_u32_e32 v34, v34, v84
	v_add_u32_e32 v35, v35, v85
	v_mad_u32_u24 v36, v84, s3, v36
	v_mad_u32_u24 v37, v85, s3, v37
	v_add_u32_e32 v39, 0x45920, v38
	global_load_dwordx2 v[84:85], v39, s[10:11]
	s_waitcnt vmcnt(42)
	s_cmp_gt_u32 s24, 23
	s_cselect_b32 s3, 1, 0
	v_add_u32_e32 v34, v34, v86
	v_add_u32_e32 v35, v35, v87
	v_mad_u32_u24 v36, v86, s3, v36
	v_mad_u32_u24 v37, v87, s3, v37
	v_add_u32_e32 v39, 0x46a40, v38
	global_load_dwordx2 v[86:87], v39, s[10:11]
	s_waitcnt vmcnt(42)
	s_cmp_gt_u32 s24, 24
	s_cselect_b32 s3, 1, 0
	v_add_u32_e32 v34, v34, v88
	v_add_u32_e32 v35, v35, v89
	v_mad_u32_u24 v36, v88, s3, v36
	v_mad_u32_u24 v37, v89, s3, v37
	v_add_u32_e32 v39, 0x47b60, v38
	global_load_dwordx2 v[88:89], v39, s[10:11]
	s_waitcnt vmcnt(42)
	s_cmp_gt_u32 s24, 25
	s_cselect_b32 s3, 1, 0
	v_add_u32_e32 v34, v34, v90
	v_add_u32_e32 v35, v35, v91
	v_mad_u32_u24 v36, v90, s3, v36
	v_mad_u32_u24 v37, v91, s3, v37
	v_add_u32_e32 v39, 0x48c80, v38
	global_load_dwordx2 v[90:91], v39, s[10:11]
	s_waitcnt vmcnt(42)
	s_cmp_gt_u32 s24, 26
	s_cselect_b32 s3, 1, 0
	v_add_u32_e32 v34, v34, v92
	v_add_u32_e32 v35, v35, v93
	v_mad_u32_u24 v36, v92, s3, v36
	v_mad_u32_u24 v37, v93, s3, v37
	v_add_u32_e32 v39, 0x49da0, v38
	global_load_dwordx2 v[92:93], v39, s[10:11]
	s_waitcnt vmcnt(42)
	s_cmp_gt_u32 s24, 27
	s_cselect_b32 s3, 1, 0
	v_add_u32_e32 v34, v34, v94
	v_add_u32_e32 v35, v35, v95
	v_mad_u32_u24 v36, v94, s3, v36
	v_mad_u32_u24 v37, v95, s3, v37
	v_add_u32_e32 v39, 0x4aec0, v38
	global_load_dwordx2 v[94:95], v39, s[10:11]
	s_waitcnt vmcnt(42)
	s_cmp_gt_u32 s24, 28
	s_cselect_b32 s3, 1, 0
	v_add_u32_e32 v34, v34, v96
	v_add_u32_e32 v35, v35, v97
	v_mad_u32_u24 v36, v96, s3, v36
	v_mad_u32_u24 v37, v97, s3, v37
	v_add_u32_e32 v39, 0x4bfe0, v38
	global_load_dwordx2 v[96:97], v39, s[10:11]
	s_waitcnt vmcnt(42)
	s_cmp_gt_u32 s24, 29
	s_cselect_b32 s3, 1, 0
	v_add_u32_e32 v34, v34, v98
	v_add_u32_e32 v35, v35, v99
	v_mad_u32_u24 v36, v98, s3, v36
	v_mad_u32_u24 v37, v99, s3, v37
	v_add_u32_e32 v39, 0x4d100, v38
	global_load_dwordx2 v[98:99], v39, s[10:11]
	s_waitcnt vmcnt(42)
	s_cmp_gt_u32 s24, 30
	s_cselect_b32 s3, 1, 0
	v_add_u32_e32 v34, v34, v100
	v_add_u32_e32 v35, v35, v101
	v_mad_u32_u24 v36, v100, s3, v36
	v_mad_u32_u24 v37, v101, s3, v37
	v_add_u32_e32 v39, 0x4e220, v38
	global_load_dwordx2 v[100:101], v39, s[10:11]
	s_waitcnt vmcnt(42)
	s_cmp_gt_u32 s24, 31
	s_cselect_b32 s3, 1, 0
	v_add_u32_e32 v34, v34, v102
	v_add_u32_e32 v35, v35, v103
	v_mad_u32_u24 v36, v102, s3, v36
	v_mad_u32_u24 v37, v103, s3, v37
	v_add_u32_e32 v39, 0x4f340, v38
	global_load_dwordx2 v[102:103], v39, s[10:11]
	s_waitcnt vmcnt(42)
	s_cmp_gt_u32 s24, 32
	s_cselect_b32 s3, 1, 0
	v_add_u32_e32 v34, v34, v104
	v_add_u32_e32 v35, v35, v105
	v_mad_u32_u24 v36, v104, s3, v36
	v_mad_u32_u24 v37, v105, s3, v37
	v_add_u32_e32 v39, 0x50460, v38
	global_load_dwordx2 v[104:105], v39, s[10:11]
	s_waitcnt vmcnt(42)
	s_cmp_gt_u32 s24, 33
	s_cselect_b32 s3, 1, 0
	v_add_u32_e32 v34, v34, v106
	v_add_u32_e32 v35, v35, v107
	v_mad_u32_u24 v36, v106, s3, v36
	v_mad_u32_u24 v37, v107, s3, v37
	v_add_u32_e32 v39, 0x51580, v38
	global_load_dwordx2 v[106:107], v39, s[10:11]
	s_waitcnt vmcnt(42)
	s_cmp_gt_u32 s24, 34
	s_cselect_b32 s3, 1, 0
	v_add_u32_e32 v34, v34, v108
	v_add_u32_e32 v35, v35, v109
	v_mad_u32_u24 v36, v108, s3, v36
	v_mad_u32_u24 v37, v109, s3, v37
	v_add_u32_e32 v39, 0x526a0, v38
	global_load_dwordx2 v[108:109], v39, s[10:11]
	s_waitcnt vmcnt(42)
	s_cmp_gt_u32 s24, 35
	s_cselect_b32 s3, 1, 0
	v_add_u32_e32 v34, v34, v110
	v_add_u32_e32 v35, v35, v111
	v_mad_u32_u24 v36, v110, s3, v36
	v_mad_u32_u24 v37, v111, s3, v37
	v_add_u32_e32 v39, 0x537c0, v38
	global_load_dwordx2 v[110:111], v39, s[10:11]
	s_waitcnt vmcnt(42)
	s_cmp_gt_u32 s24, 36
	s_cselect_b32 s3, 1, 0
	v_add_u32_e32 v34, v34, v112
	v_add_u32_e32 v35, v35, v113
	v_mad_u32_u24 v36, v112, s3, v36
	v_mad_u32_u24 v37, v113, s3, v37
	v_add_u32_e32 v39, 0x548e0, v38
	global_load_dwordx2 v[112:113], v39, s[10:11]
	s_waitcnt vmcnt(42)
	s_cmp_gt_u32 s24, 37
	s_cselect_b32 s3, 1, 0
	v_add_u32_e32 v34, v34, v114
	v_add_u32_e32 v35, v35, v115
	v_mad_u32_u24 v36, v114, s3, v36
	v_mad_u32_u24 v37, v115, s3, v37
	v_add_u32_e32 v39, 0x55a00, v38
	global_load_dwordx2 v[114:115], v39, s[10:11]
	s_waitcnt vmcnt(42)
	s_cmp_gt_u32 s24, 38
	s_cselect_b32 s3, 1, 0
	v_add_u32_e32 v34, v34, v116
	v_add_u32_e32 v35, v35, v117
	v_mad_u32_u24 v36, v116, s3, v36
	v_mad_u32_u24 v37, v117, s3, v37
	v_add_u32_e32 v39, 0x56b20, v38
	global_load_dwordx2 v[116:117], v39, s[10:11]
	s_waitcnt vmcnt(42)
	s_cmp_gt_u32 s24, 39
	s_cselect_b32 s3, 1, 0
	v_add_u32_e32 v34, v34, v118
	v_add_u32_e32 v35, v35, v119
	v_mad_u32_u24 v36, v118, s3, v36
	v_mad_u32_u24 v37, v119, s3, v37
	v_add_u32_e32 v39, 0x57c40, v38
	global_load_dwordx2 v[118:119], v39, s[10:11]
	s_waitcnt vmcnt(42)
	s_cmp_gt_u32 s24, 40
	s_cselect_b32 s3, 1, 0
	v_add_u32_e32 v34, v34, v120
	v_add_u32_e32 v35, v35, v121
	v_mad_u32_u24 v36, v120, s3, v36
	v_mad_u32_u24 v37, v121, s3, v37
	v_add_u32_e32 v39, 0x58d60, v38
	global_load_dwordx2 v[120:121], v39, s[10:11]
	s_waitcnt vmcnt(42)
	s_cmp_gt_u32 s24, 41
	s_cselect_b32 s3, 1, 0
	v_add_u32_e32 v34, v34, v122
	v_add_u32_e32 v35, v35, v123
	v_mad_u32_u24 v36, v122, s3, v36
	v_mad_u32_u24 v37, v123, s3, v37
	v_add_u32_e32 v39, 0x59e80, v38
	global_load_dwordx2 v[122:123], v39, s[10:11]
	s_waitcnt vmcnt(42)
	s_cmp_gt_u32 s24, 42
	s_cselect_b32 s3, 1, 0
	v_add_u32_e32 v34, v34, v124
	v_add_u32_e32 v35, v35, v125
	v_mad_u32_u24 v36, v124, s3, v36
	v_mad_u32_u24 v37, v125, s3, v37
	v_add_u32_e32 v39, 0x5afa0, v38
	global_load_dwordx2 v[124:125], v39, s[10:11]
	s_waitcnt vmcnt(42)
	s_cmp_gt_u32 s24, 43
	s_cselect_b32 s3, 1, 0
	v_add_u32_e32 v34, v34, v40
	v_add_u32_e32 v35, v35, v41
	v_mad_u32_u24 v36, v40, s3, v36
	v_mad_u32_u24 v37, v41, s3, v37
	s_waitcnt vmcnt(41)
	s_cmp_gt_u32 s24, 44
	s_cselect_b32 s3, 1, 0
	v_add_u32_e32 v34, v34, v42
	v_add_u32_e32 v35, v35, v43
	v_mad_u32_u24 v36, v42, s3, v36
	v_mad_u32_u24 v37, v43, s3, v37
	s_waitcnt vmcnt(40)
	s_cmp_gt_u32 s24, 45
	s_cselect_b32 s3, 1, 0
	v_add_u32_e32 v34, v34, v44
	v_add_u32_e32 v35, v35, v45
	v_mad_u32_u24 v36, v44, s3, v36
	v_mad_u32_u24 v37, v45, s3, v37
	s_waitcnt vmcnt(39)
	s_cmp_gt_u32 s24, 46
	s_cselect_b32 s3, 1, 0
	v_add_u32_e32 v34, v34, v46
	v_add_u32_e32 v35, v35, v47
	v_mad_u32_u24 v36, v46, s3, v36
	v_mad_u32_u24 v37, v47, s3, v37
	s_waitcnt vmcnt(38)
	s_cmp_gt_u32 s24, 47
	s_cselect_b32 s3, 1, 0
	v_add_u32_e32 v34, v34, v48
	v_add_u32_e32 v35, v35, v49
	v_mad_u32_u24 v36, v48, s3, v36
	v_mad_u32_u24 v37, v49, s3, v37
	s_waitcnt vmcnt(37)
	s_cmp_gt_u32 s24, 48
	s_cselect_b32 s3, 1, 0
	v_add_u32_e32 v34, v34, v50
	v_add_u32_e32 v35, v35, v51
	v_mad_u32_u24 v36, v50, s3, v36
	v_mad_u32_u24 v37, v51, s3, v37
	s_waitcnt vmcnt(36)
	s_cmp_gt_u32 s24, 49
	s_cselect_b32 s3, 1, 0
	v_add_u32_e32 v34, v34, v52
	v_add_u32_e32 v35, v35, v53
	v_mad_u32_u24 v36, v52, s3, v36
	v_mad_u32_u24 v37, v53, s3, v37
	s_waitcnt vmcnt(35)
	s_cmp_gt_u32 s24, 50
	s_cselect_b32 s3, 1, 0
	v_add_u32_e32 v34, v34, v54
	v_add_u32_e32 v35, v35, v55
	v_mad_u32_u24 v36, v54, s3, v36
	v_mad_u32_u24 v37, v55, s3, v37
	s_waitcnt vmcnt(34)
	s_cmp_gt_u32 s24, 51
	s_cselect_b32 s3, 1, 0
	v_add_u32_e32 v34, v34, v56
	v_add_u32_e32 v35, v35, v57
	v_mad_u32_u24 v36, v56, s3, v36
	v_mad_u32_u24 v37, v57, s3, v37
	s_waitcnt vmcnt(33)
	s_cmp_gt_u32 s24, 52
	s_cselect_b32 s3, 1, 0
	v_add_u32_e32 v34, v34, v58
	v_add_u32_e32 v35, v35, v59
	v_mad_u32_u24 v36, v58, s3, v36
	v_mad_u32_u24 v37, v59, s3, v37
	s_waitcnt vmcnt(32)
	s_cmp_gt_u32 s24, 53
	s_cselect_b32 s3, 1, 0
	v_add_u32_e32 v34, v34, v60
	v_add_u32_e32 v35, v35, v61
	v_mad_u32_u24 v36, v60, s3, v36
	v_mad_u32_u24 v37, v61, s3, v37
	s_waitcnt vmcnt(31)
	s_cmp_gt_u32 s24, 54
	s_cselect_b32 s3, 1, 0
	v_add_u32_e32 v34, v34, v62
	v_add_u32_e32 v35, v35, v63
	v_mad_u32_u24 v36, v62, s3, v36
	v_mad_u32_u24 v37, v63, s3, v37
	s_waitcnt vmcnt(30)
	s_cmp_gt_u32 s24, 55
	s_cselect_b32 s3, 1, 0
	v_add_u32_e32 v34, v34, v64
	v_add_u32_e32 v35, v35, v65
	v_mad_u32_u24 v36, v64, s3, v36
	v_mad_u32_u24 v37, v65, s3, v37
	s_waitcnt vmcnt(29)
	s_cmp_gt_u32 s24, 56
	s_cselect_b32 s3, 1, 0
	v_add_u32_e32 v34, v34, v66
	v_add_u32_e32 v35, v35, v67
	v_mad_u32_u24 v36, v66, s3, v36
	v_mad_u32_u24 v37, v67, s3, v37
	s_waitcnt vmcnt(28)
	s_cmp_gt_u32 s24, 57
	s_cselect_b32 s3, 1, 0
	v_add_u32_e32 v34, v34, v68
	v_add_u32_e32 v35, v35, v69
	v_mad_u32_u24 v36, v68, s3, v36
	v_mad_u32_u24 v37, v69, s3, v37
	s_waitcnt vmcnt(27)
	s_cmp_gt_u32 s24, 58
	s_cselect_b32 s3, 1, 0
	v_add_u32_e32 v34, v34, v70
	v_add_u32_e32 v35, v35, v71
	v_mad_u32_u24 v36, v70, s3, v36
	v_mad_u32_u24 v37, v71, s3, v37
	s_waitcnt vmcnt(26)
	s_cmp_gt_u32 s24, 59
	s_cselect_b32 s3, 1, 0
	v_add_u32_e32 v34, v34, v72
	v_add_u32_e32 v35, v35, v73
	v_mad_u32_u24 v36, v72, s3, v36
	v_mad_u32_u24 v37, v73, s3, v37
	s_waitcnt vmcnt(25)
	s_cmp_gt_u32 s24, 60
	s_cselect_b32 s3, 1, 0
	v_add_u32_e32 v34, v34, v74
	v_add_u32_e32 v35, v35, v75
	v_mad_u32_u24 v36, v74, s3, v36
	v_mad_u32_u24 v37, v75, s3, v37
	s_waitcnt vmcnt(24)
	s_cmp_gt_u32 s24, 61
	s_cselect_b32 s3, 1, 0
	v_add_u32_e32 v34, v34, v76
	v_add_u32_e32 v35, v35, v77
	v_mad_u32_u24 v36, v76, s3, v36
	v_mad_u32_u24 v37, v77, s3, v37
	s_waitcnt vmcnt(23)
	s_cmp_gt_u32 s24, 62
	s_cselect_b32 s3, 1, 0
	v_add_u32_e32 v34, v34, v78
	v_add_u32_e32 v35, v35, v79
	v_mad_u32_u24 v36, v78, s3, v36
	v_mad_u32_u24 v37, v79, s3, v37
	s_waitcnt vmcnt(22)
	s_cmp_gt_u32 s24, 63
	s_cselect_b32 s3, 1, 0
	v_add_u32_e32 v34, v34, v80
	v_add_u32_e32 v35, v35, v81
	v_mad_u32_u24 v36, v80, s3, v36
	v_mad_u32_u24 v37, v81, s3, v37
	s_waitcnt vmcnt(21)
	s_cmp_gt_u32 s24, 64
	s_cselect_b32 s3, 1, 0
	v_add_u32_e32 v34, v34, v82
	v_add_u32_e32 v35, v35, v83
	v_mad_u32_u24 v36, v82, s3, v36
	v_mad_u32_u24 v37, v83, s3, v37
	s_waitcnt vmcnt(20)
	s_cmp_gt_u32 s24, 65
	s_cselect_b32 s3, 1, 0
	v_add_u32_e32 v34, v34, v84
	v_add_u32_e32 v35, v35, v85
	v_mad_u32_u24 v36, v84, s3, v36
	v_mad_u32_u24 v37, v85, s3, v37
	s_waitcnt vmcnt(19)
	s_cmp_gt_u32 s24, 66
	s_cselect_b32 s3, 1, 0
	v_add_u32_e32 v34, v34, v86
	v_add_u32_e32 v35, v35, v87
	v_mad_u32_u24 v36, v86, s3, v36
	v_mad_u32_u24 v37, v87, s3, v37
	s_waitcnt vmcnt(18)
	s_cmp_gt_u32 s24, 67
	s_cselect_b32 s3, 1, 0
	v_add_u32_e32 v34, v34, v88
	v_add_u32_e32 v35, v35, v89
	v_mad_u32_u24 v36, v88, s3, v36
	v_mad_u32_u24 v37, v89, s3, v37
	s_waitcnt vmcnt(17)
	s_cmp_gt_u32 s24, 68
	s_cselect_b32 s3, 1, 0
	v_add_u32_e32 v34, v34, v90
	v_add_u32_e32 v35, v35, v91
	v_mad_u32_u24 v36, v90, s3, v36
	v_mad_u32_u24 v37, v91, s3, v37
	s_waitcnt vmcnt(16)
	s_cmp_gt_u32 s24, 69
	s_cselect_b32 s3, 1, 0
	v_add_u32_e32 v34, v34, v92
	v_add_u32_e32 v35, v35, v93
	v_mad_u32_u24 v36, v92, s3, v36
	v_mad_u32_u24 v37, v93, s3, v37
	s_waitcnt vmcnt(15)
	s_cmp_gt_u32 s24, 70
	s_cselect_b32 s3, 1, 0
	v_add_u32_e32 v34, v34, v94
	v_add_u32_e32 v35, v35, v95
	v_mad_u32_u24 v36, v94, s3, v36
	v_mad_u32_u24 v37, v95, s3, v37
	s_waitcnt vmcnt(14)
	s_cmp_gt_u32 s24, 71
	s_cselect_b32 s3, 1, 0
	v_add_u32_e32 v34, v34, v96
	v_add_u32_e32 v35, v35, v97
	v_mad_u32_u24 v36, v96, s3, v36
	v_mad_u32_u24 v37, v97, s3, v37
	s_waitcnt vmcnt(13)
	s_cmp_gt_u32 s24, 72
	s_cselect_b32 s3, 1, 0
	v_add_u32_e32 v34, v34, v98
	v_add_u32_e32 v35, v35, v99
	v_mad_u32_u24 v36, v98, s3, v36
	v_mad_u32_u24 v37, v99, s3, v37
	s_waitcnt vmcnt(12)
	s_cmp_gt_u32 s24, 73
	s_cselect_b32 s3, 1, 0
	v_add_u32_e32 v34, v34, v100
	v_add_u32_e32 v35, v35, v101
	v_mad_u32_u24 v36, v100, s3, v36
	v_mad_u32_u24 v37, v101, s3, v37
	s_waitcnt vmcnt(11)
	s_cmp_gt_u32 s24, 74
	s_cselect_b32 s3, 1, 0
	v_add_u32_e32 v34, v34, v102
	v_add_u32_e32 v35, v35, v103
	v_mad_u32_u24 v36, v102, s3, v36
	v_mad_u32_u24 v37, v103, s3, v37
	s_waitcnt vmcnt(10)
	s_cmp_gt_u32 s24, 75
	s_cselect_b32 s3, 1, 0
	v_add_u32_e32 v34, v34, v104
	v_add_u32_e32 v35, v35, v105
	v_mad_u32_u24 v36, v104, s3, v36
	v_mad_u32_u24 v37, v105, s3, v37
	s_waitcnt vmcnt(9)
	s_cmp_gt_u32 s24, 76
	s_cselect_b32 s3, 1, 0
	v_add_u32_e32 v34, v34, v106
	v_add_u32_e32 v35, v35, v107
	v_mad_u32_u24 v36, v106, s3, v36
	v_mad_u32_u24 v37, v107, s3, v37
	s_waitcnt vmcnt(8)
	s_cmp_gt_u32 s24, 77
	s_cselect_b32 s3, 1, 0
	v_add_u32_e32 v34, v34, v108
	v_add_u32_e32 v35, v35, v109
	v_mad_u32_u24 v36, v108, s3, v36
	v_mad_u32_u24 v37, v109, s3, v37
	s_waitcnt vmcnt(7)
	s_cmp_gt_u32 s24, 78
	s_cselect_b32 s3, 1, 0
	v_add_u32_e32 v34, v34, v110
	v_add_u32_e32 v35, v35, v111
	v_mad_u32_u24 v36, v110, s3, v36
	v_mad_u32_u24 v37, v111, s3, v37
	s_waitcnt vmcnt(6)
	s_cmp_gt_u32 s24, 79
	s_cselect_b32 s3, 1, 0
	v_add_u32_e32 v34, v34, v112
	v_add_u32_e32 v35, v35, v113
	v_mad_u32_u24 v36, v112, s3, v36
	v_mad_u32_u24 v37, v113, s3, v37
	s_waitcnt vmcnt(5)
	s_cmp_gt_u32 s24, 80
	s_cselect_b32 s3, 1, 0
	v_add_u32_e32 v34, v34, v114
	v_add_u32_e32 v35, v35, v115
	v_mad_u32_u24 v36, v114, s3, v36
	v_mad_u32_u24 v37, v115, s3, v37
	s_waitcnt vmcnt(4)
	s_cmp_gt_u32 s24, 81
	s_cselect_b32 s3, 1, 0
	v_add_u32_e32 v34, v34, v116
	v_add_u32_e32 v35, v35, v117
	v_mad_u32_u24 v36, v116, s3, v36
	v_mad_u32_u24 v37, v117, s3, v37
	s_waitcnt vmcnt(3)
	s_cmp_gt_u32 s24, 82
	s_cselect_b32 s3, 1, 0
	v_add_u32_e32 v34, v34, v118
	v_add_u32_e32 v35, v35, v119
	v_mad_u32_u24 v36, v118, s3, v36
	v_mad_u32_u24 v37, v119, s3, v37
	s_waitcnt vmcnt(2)
	s_cmp_gt_u32 s24, 83
	s_cselect_b32 s3, 1, 0
	v_add_u32_e32 v34, v34, v120
	v_add_u32_e32 v35, v35, v121
	v_mad_u32_u24 v36, v120, s3, v36
	v_mad_u32_u24 v37, v121, s3, v37
	s_waitcnt vmcnt(1)
	s_cmp_gt_u32 s24, 84
	s_cselect_b32 s3, 1, 0
	v_add_u32_e32 v34, v34, v122
	v_add_u32_e32 v35, v35, v123
	v_mad_u32_u24 v36, v122, s3, v36
	v_mad_u32_u24 v37, v123, s3, v37
	s_waitcnt vmcnt(0)
	s_cmp_gt_u32 s24, 85
	s_cselect_b32 s3, 1, 0
	v_add_u32_e32 v34, v34, v124
	v_add_u32_e32 v35, v35, v125
	v_mad_u32_u24 v36, v124, s3, v36
	v_mad_u32_u24 v37, v125, s3, v37

.Lsc_dskip15:
	s_waitcnt lgkmcnt(0)
	s_barrier
	v_lshlrev_b32_e32 v50, 3, v0
	v_mov_b32_e32 v52, 0
	v_mov_b32_e32 v53, 0
	v_cmp_gt_u32_e32 vcc, 0x224, v0
	s_and_saveexec_b64 s[36:37], vcc
	ds_read_b64 v[52:53], v50 offset:4608
	s_mov_b64 exec, s[36:37]
	s_waitcnt lgkmcnt(0)
	v_add_u32_e32 v54, v52, v53
	v_mov_b32_e32 v55, v54
	s_nop 1
	v_add_u32_dpp v55, v55, v55 row_shr:1 row_mask:0xf bank_mask:0xf bound_ctrl:0
	s_nop 1
	v_add_u32_dpp v55, v55, v55 row_shr:2 row_mask:0xf bank_mask:0xf bound_ctrl:0
	s_nop 1
	v_add_u32_dpp v55, v55, v55 row_shr:4 row_mask:0xf bank_mask:0xf bound_ctrl:0
	s_nop 1
	v_add_u32_dpp v55, v55, v55 row_shr:8 row_mask:0xf bank_mask:0xf bound_ctrl:0
	s_nop 1
	v_add_u32_dpp v55, v55, v55 row_bcast:15 row_mask:0xa bank_mask:0xf
	s_nop 1
	v_add_u32_dpp v55, v55, v55 row_bcast:31 row_mask:0xc bank_mask:0xf
	v_lshrrev_b32_e32 v56, 6, v0
	s_nop 0
	v_readfirstlane_b32 s3, v56
	v_readlane_b32 s14, v55, 63
	s_lshl_b32 s15, s3, 2
	s_add_u32 s15, s15, 0x2400
	v_mov_b32_e32 v57, s14
	v_mov_b32_e32 v58, s15
	s_mov_b64 s[38:39], exec
	s_mov_b64 exec, 1
	ds_write_b32 v58, v57
	s_mov_b64 exec, s[38:39]
	s_waitcnt lgkmcnt(0)
	s_barrier
	v_and_b32_e32 v57, 15, v0
	v_lshlrev_b32_e32 v57, 2, v57
	ds_read_b32 v57, v57 offset:9216
	s_waitcnt lgkmcnt(0)
	s_nop 1
	v_add_u32_dpp v57, v57, v57 row_shr:1 row_mask:0xf bank_mask:0xf bound_ctrl:0
	s_nop 1
	v_add_u32_dpp v57, v57, v57 row_shr:2 row_mask:0xf bank_mask:0xf bound_ctrl:0
	s_nop 1
	v_add_u32_dpp v57, v57, v57 row_shr:4 row_mask:0xf bank_mask:0xf bound_ctrl:0
	s_nop 1
	v_add_u32_dpp v57, v57, v57 row_shr:8 row_mask:0xf bank_mask:0xf bound_ctrl:0
	s_sub_u32 s15, s3, 1
	s_max_i32 s15, s15, 0
	s_nop 1
	v_readlane_b32 s16, v57, s15
	s_cmp_eq_u32 s3, 0
	s_cselect_b32 s16, 0, s16
	v_sub_u32_e32 v58, v55, v54
	v_add_u32_e32 v58, s16, v58
	v_add_u32_e32 v59, v58, v52
	v_cmp_gt_u32_e32 vcc, 0x224, v0
	s_and_saveexec_b64 s[36:37], vcc
	ds_read_b64 v[56:57], v50
	ds_write_b64 v50, v[58:59] offset:9728
	s_waitcnt lgkmcnt(0)
	v_sub_u32_e32 v56, v56, v58
	v_sub_u32_e32 v57, v57, v59
	ds_write_b64 v50, v[56:57]
	s_mov_b64 exec, s[36:37]
	s_waitcnt lgkmcnt(0)
	s_barrier
	v_mov_b32_e32 v60, 0x447
	v_cmp_gt_i32_e64 s[20:21], 0, v3
	v_subrev_co_u32_e32 v51, vcc, 0x61a80, v3
	v_lshrrev_b32_e32 v51, 6, v51
	v_lshrrev_b32_e32 v52, 9, v3
	v_add_u32_e32 v51, 0x30e, v51
	v_cndmask_b32_e32 v51, v51, v52, vcc
	v_cndmask_b32_e64 v51, v51, v60, s[20:21]
	v_lshlrev_b32_e32 v51, 2, v51
	ds_read_b32 v53, v51 offset:9728
	v_cmp_gt_i32_e64 s[20:21], 0, v5
	v_subrev_co_u32_e32 v51, vcc, 0x61a80, v5
	v_lshrrev_b32_e32 v51, 6, v51
	v_lshrrev_b32_e32 v52, 9, v5
	v_add_u32_e32 v51, 0x30e, v51
	v_cndmask_b32_e32 v51, v51, v52, vcc
	v_cndmask_b32_e64 v51, v51, v60, s[20:21]
	v_lshlrev_b32_e32 v51, 2, v51
	ds_read_b32 v54, v51 offset:9728
	v_cmp_gt_i32_e64 s[20:21], 0, v7
	v_subrev_co_u32_e32 v51, vcc, 0x61a80, v7
	v_lshrrev_b32_e32 v51, 6, v51
	v_lshrrev_b32_e32 v52, 9, v7
	v_add_u32_e32 v51, 0x30e, v51
	v_cndmask_b32_e32 v51, v51, v52, vcc
	v_cndmask_b32_e64 v51, v51, v60, s[20:21]
	v_lshlrev_b32_e32 v51, 2, v51
	ds_read_b32 v55, v51 offset:9728
	v_cmp_gt_i32_e64 s[20:21], 0, v9
	v_subrev_co_u32_e32 v51, vcc, 0x61a80, v9
	v_lshrrev_b32_e32 v51, 6, v51
	v_lshrrev_b32_e32 v52, 9, v9
	v_add_u32_e32 v51, 0x30e, v51
	v_cndmask_b32_e32 v51, v51, v52, vcc
	v_cndmask_b32_e64 v51, v51, v60, s[20:21]
	v_lshlrev_b32_e32 v51, 2, v51
	ds_read_b32 v56, v51 offset:9728
	s_waitcnt lgkmcnt(0)
	v_add_u32_e32 v34, v34, v53
	v_add_u32_e32 v35, v35, v54
	v_add_u32_e32 v36, v36, v55
	v_add_u32_e32 v37, v37, v56
	v_cmp_gt_i32_e64 s[20:21], 0, v11
	v_subrev_co_u32_e32 v51, vcc, 0x61a80, v11
	v_lshrrev_b32_e32 v51, 6, v51
	v_lshrrev_b32_e32 v52, 9, v11
	v_add_u32_e32 v51, 0x30e, v51
	v_cndmask_b32_e32 v51, v51, v52, vcc
	v_cndmask_b32_e64 v51, v51, v60, s[20:21]
	v_lshlrev_b32_e32 v51, 2, v51
	ds_read_b32 v53, v51 offset:9728
	v_cmp_gt_i32_e64 s[20:21], 0, v13
	v_subrev_co_u32_e32 v51, vcc, 0x61a80, v13
	v_lshrrev_b32_e32 v51, 6, v51
	v_lshrrev_b32_e32 v52, 9, v13
	v_add_u32_e32 v51, 0x30e, v51
	v_cndmask_b32_e32 v51, v51, v52, vcc
	v_cndmask_b32_e64 v51, v51, v60, s[20:21]
	v_lshlrev_b32_e32 v51, 2, v51
	ds_read_b32 v54, v51 offset:9728
	v_cmp_gt_i32_e64 s[20:21], 0, v15
	v_subrev_co_u32_e32 v51, vcc, 0x61a80, v15
	v_lshrrev_b32_e32 v51, 6, v51
	v_lshrrev_b32_e32 v52, 9, v15
	v_add_u32_e32 v51, 0x30e, v51
	v_cndmask_b32_e32 v51, v51, v52, vcc
	v_cndmask_b32_e64 v51, v51, v60, s[20:21]
	v_lshlrev_b32_e32 v51, 2, v51
	ds_read_b32 v55, v51 offset:9728
	v_cmp_gt_i32_e64 s[20:21], 0, v17
	v_subrev_co_u32_e32 v51, vcc, 0x61a80, v17
	v_lshrrev_b32_e32 v51, 6, v51
	v_lshrrev_b32_e32 v52, 9, v17
	v_add_u32_e32 v51, 0x30e, v51
	v_cndmask_b32_e32 v51, v51, v52, vcc
	v_cndmask_b32_e64 v51, v51, v60, s[20:21]
	v_lshlrev_b32_e32 v51, 2, v51
	ds_read_b32 v56, v51 offset:9728
	s_waitcnt lgkmcnt(0)
	v_add_u32_e32 v38, v38, v53
	v_add_u32_e32 v39, v39, v54
	v_add_u32_e32 v40, v40, v55
	v_add_u32_e32 v41, v41, v56
	v_cmp_gt_i32_e64 s[20:21], 0, v19
	v_subrev_co_u32_e32 v51, vcc, 0x61a80, v19
	v_lshrrev_b32_e32 v51, 6, v51
	v_lshrrev_b32_e32 v52, 9, v19
	v_add_u32_e32 v51, 0x30e, v51
	v_cndmask_b32_e32 v51, v51, v52, vcc
	v_cndmask_b32_e64 v51, v51, v60, s[20:21]
	v_lshlrev_b32_e32 v51, 2, v51
	ds_read_b32 v53, v51 offset:9728
	v_cmp_gt_i32_e64 s[20:21], 0, v21
	v_subrev_co_u32_e32 v51, vcc, 0x61a80, v21
	v_lshrrev_b32_e32 v51, 6, v51
	v_lshrrev_b32_e32 v52, 9, v21
	v_add_u32_e32 v51, 0x30e, v51
	v_cndmask_b32_e32 v51, v51, v52, vcc
	v_cndmask_b32_e64 v51, v51, v60, s[20:21]
	v_lshlrev_b32_e32 v51, 2, v51
	ds_read_b32 v54, v51 offset:9728
	v_cmp_gt_i32_e64 s[20:21], 0, v23
	v_subrev_co_u32_e32 v51, vcc, 0x61a80, v23
	v_lshrrev_b32_e32 v51, 6, v51
	v_lshrrev_b32_e32 v52, 9, v23
	v_add_u32_e32 v51, 0x30e, v51
	v_cndmask_b32_e32 v51, v51, v52, vcc
	v_cndmask_b32_e64 v51, v51, v60, s[20:21]
	v_lshlrev_b32_e32 v51, 2, v51
	ds_read_b32 v55, v51 offset:9728
	v_cmp_gt_i32_e64 s[20:21], 0, v25
	v_subrev_co_u32_e32 v51, vcc, 0x61a80, v25
	v_lshrrev_b32_e32 v51, 6, v51
	v_lshrrev_b32_e32 v52, 9, v25
	v_add_u32_e32 v51, 0x30e, v51
	v_cndmask_b32_e32 v51, v51, v52, vcc
	v_cndmask_b32_e64 v51, v51, v60, s[20:21]
	v_lshlrev_b32_e32 v51, 2, v51
	ds_read_b32 v56, v51 offset:9728
	s_waitcnt lgkmcnt(0)
	v_add_u32_e32 v42, v42, v53
	v_add_u32_e32 v43, v43, v54
	v_add_u32_e32 v44, v44, v55
	v_add_u32_e32 v45, v45, v56
	v_cmp_gt_i32_e64 s[20:21], 0, v27
	v_subrev_co_u32_e32 v51, vcc, 0x61a80, v27
	v_lshrrev_b32_e32 v51, 6, v51
	v_lshrrev_b32_e32 v52, 9, v27
	v_add_u32_e32 v51, 0x30e, v51
	v_cndmask_b32_e32 v51, v51, v52, vcc
	v_cndmask_b32_e64 v51, v51, v60, s[20:21]
	v_lshlrev_b32_e32 v51, 2, v51
	ds_read_b32 v53, v51 offset:9728
	v_cmp_gt_i32_e64 s[20:21], 0, v29
	v_subrev_co_u32_e32 v51, vcc, 0x61a80, v29
	v_lshrrev_b32_e32 v51, 6, v51
	v_lshrrev_b32_e32 v52, 9, v29
	v_add_u32_e32 v51, 0x30e, v51
	v_cndmask_b32_e32 v51, v51, v52, vcc
	v_cndmask_b32_e64 v51, v51, v60, s[20:21]
	v_lshlrev_b32_e32 v51, 2, v51
	ds_read_b32 v54, v51 offset:9728
	v_cmp_gt_i32_e64 s[20:21], 0, v31
	v_subrev_co_u32_e32 v51, vcc, 0x61a80, v31
	v_lshrrev_b32_e32 v51, 6, v51
	v_lshrrev_b32_e32 v52, 9, v31
	v_add_u32_e32 v51, 0x30e, v51
	v_cndmask_b32_e32 v51, v51, v52, vcc
	v_cndmask_b32_e64 v51, v51, v60, s[20:21]
	v_lshlrev_b32_e32 v51, 2, v51
	ds_read_b32 v55, v51 offset:9728
	v_cmp_gt_i32_e64 s[20:21], 0, v33
	v_subrev_co_u32_e32 v51, vcc, 0x61a80, v33
	v_lshrrev_b32_e32 v51, 6, v51
	v_lshrrev_b32_e32 v52, 9, v33
	v_add_u32_e32 v51, 0x30e, v51
	v_cndmask_b32_e32 v51, v51, v52, vcc
	v_cndmask_b32_e64 v51, v51, v60, s[20:21]
	v_lshlrev_b32_e32 v51, 2, v51
	ds_read_b32 v56, v51 offset:9728
	s_waitcnt lgkmcnt(0)
	v_add_u32_e32 v46, v46, v53
	v_add_u32_e32 v47, v47, v54
	v_add_u32_e32 v48, v48, v55
	v_add_u32_e32 v49, v49, v56
	s_mov_b64 s[38:39], exec
	s_movk_i32 s14, 0x2000
	v_cmp_gt_u32_e32 vcc, s14, v34
	v_lshlrev_b32_e32 v52, 3, v34
	s_and_b64 exec, s[38:39], vcc
	ds_write_b64 v52, v[2:3] offset:14336
	s_mov_b64 exec, s[38:39]
	v_cmp_gt_u32_e32 vcc, s14, v35
	v_lshlrev_b32_e32 v52, 3, v35
	s_and_b64 exec, s[38:39], vcc
	ds_write_b64 v52, v[4:5] offset:14336
	s_mov_b64 exec, s[38:39]
	v_cmp_gt_u32_e32 vcc, s14, v36
	v_lshlrev_b32_e32 v52, 3, v36
	s_and_b64 exec, s[38:39], vcc
	ds_write_b64 v52, v[6:7] offset:14336
	s_mov_b64 exec, s[38:39]
	v_cmp_gt_u32_e32 vcc, s14, v37
	v_lshlrev_b32_e32 v52, 3, v37
	s_and_b64 exec, s[38:39], vcc
	ds_write_b64 v52, v[8:9] offset:14336
	s_mov_b64 exec, s[38:39]
	v_cmp_gt_u32_e32 vcc, s14, v38
	v_lshlrev_b32_e32 v52, 3, v38
	s_and_b64 exec, s[38:39], vcc
	ds_write_b64 v52, v[10:11] offset:14336
	s_mov_b64 exec, s[38:39]
	v_cmp_gt_u32_e32 vcc, s14, v39
	v_lshlrev_b32_e32 v52, 3, v39
	s_and_b64 exec, s[38:39], vcc
	ds_write_b64 v52, v[12:13] offset:14336
	s_mov_b64 exec, s[38:39]
	v_cmp_gt_u32_e32 vcc, s14, v40
	v_lshlrev_b32_e32 v52, 3, v40
	s_and_b64 exec, s[38:39], vcc
	ds_write_b64 v52, v[14:15] offset:14336
	s_mov_b64 exec, s[38:39]
	v_cmp_gt_u32_e32 vcc, s14, v41
	v_lshlrev_b32_e32 v52, 3, v41
	s_and_b64 exec, s[38:39], vcc
	ds_write_b64 v52, v[16:17] offset:14336
	s_mov_b64 exec, s[38:39]
	v_cmp_gt_u32_e32 vcc, s14, v42
	v_lshlrev_b32_e32 v52, 3, v42
	s_and_b64 exec, s[38:39], vcc
	ds_write_b64 v52, v[18:19] offset:14336
	s_mov_b64 exec, s[38:39]
	v_cmp_gt_u32_e32 vcc, s14, v43
	v_lshlrev_b32_e32 v52, 3, v43
	s_and_b64 exec, s[38:39], vcc
	ds_write_b64 v52, v[20:21] offset:14336
	s_mov_b64 exec, s[38:39]
	v_cmp_gt_u32_e32 vcc, s14, v44
	v_lshlrev_b32_e32 v52, 3, v44
	s_and_b64 exec, s[38:39], vcc
	ds_write_b64 v52, v[22:23] offset:14336
	s_mov_b64 exec, s[38:39]
	v_cmp_gt_u32_e32 vcc, s14, v45
	v_lshlrev_b32_e32 v52, 3, v45
	s_and_b64 exec, s[38:39], vcc
	ds_write_b64 v52, v[24:25] offset:14336
	s_mov_b64 exec, s[38:39]
	v_cmp_gt_u32_e32 vcc, s14, v46
	v_lshlrev_b32_e32 v52, 3, v46
	s_and_b64 exec, s[38:39], vcc
	ds_write_b64 v52, v[26:27] offset:14336
	s_mov_b64 exec, s[38:39]
	v_cmp_gt_u32_e32 vcc, s14, v47
	v_lshlrev_b32_e32 v52, 3, v47
	s_and_b64 exec, s[38:39], vcc
	ds_write_b64 v52, v[28:29] offset:14336
	s_mov_b64 exec, s[38:39]
	v_cmp_gt_u32_e32 vcc, s14, v48
	v_lshlrev_b32_e32 v52, 3, v48
	s_and_b64 exec, s[38:39], vcc
	ds_write_b64 v52, v[30:31] offset:14336
	s_mov_b64 exec, s[38:39]
	v_cmp_gt_u32_e32 vcc, s14, v49
	v_lshlrev_b32_e32 v52, 3, v49
	s_and_b64 exec, s[38:39], vcc
	ds_write_b64 v52, v[32:33] offset:14336
	s_mov_b64 exec, s[38:39]
	s_waitcnt lgkmcnt(0)
	s_barrier
	v_mov_b32_e32 v61, v0
	v_lshlrev_b32_e32 v62, 3, v61
	ds_read_b64 v[50:51], v62 offset:14336
	s_waitcnt lgkmcnt(0)
	v_subrev_co_u32_e32 v53, vcc, 0x61a80, v51
	v_lshrrev_b32_e32 v53, 6, v53
	v_lshrrev_b32_e32 v54, 9, v51
	v_add_u32_e32 v53, 0x30e, v53
	v_cndmask_b32_e32 v53, v53, v54, vcc
	v_min_u32_e32 v53, 0x447, v53
	v_lshlrev_b32_e32 v53, 2, v53
	ds_read_b32 v53, v53
	v_cmp_le_i32_e32 vcc, 0, v51
	s_waitcnt lgkmcnt(0)
	v_add_u32_e32 v53, v53, v61
	v_lshlrev_b32_e32 v53, 3, v53
	s_and_b64 exec, s[38:39], vcc
	global_store_dwordx2 v53, v[50:51], s[34:35]
	s_mov_b64 exec, s[38:39]
	v_add_u32_e32 v61, 0x400, v0
	v_lshlrev_b32_e32 v62, 3, v61
	ds_read_b64 v[50:51], v62 offset:14336
	s_waitcnt lgkmcnt(0)
	v_subrev_co_u32_e32 v53, vcc, 0x61a80, v51
	v_lshrrev_b32_e32 v53, 6, v53
	v_lshrrev_b32_e32 v54, 9, v51
	v_add_u32_e32 v53, 0x30e, v53
	v_cndmask_b32_e32 v53, v53, v54, vcc
	v_min_u32_e32 v53, 0x447, v53
	v_lshlrev_b32_e32 v53, 2, v53
	ds_read_b32 v53, v53
	v_cmp_le_i32_e32 vcc, 0, v51
	s_waitcnt lgkmcnt(0)
	v_add_u32_e32 v53, v53, v61
	v_lshlrev_b32_e32 v53, 3, v53
	s_and_b64 exec, s[38:39], vcc
	global_store_dwordx2 v53, v[50:51], s[34:35]
	s_mov_b64 exec, s[38:39]
	v_add_u32_e32 v61, 0x800, v0
	v_lshlrev_b32_e32 v62, 3, v61
	ds_read_b64 v[50:51], v62 offset:14336
	s_waitcnt lgkmcnt(0)
	v_subrev_co_u32_e32 v53, vcc, 0x61a80, v51
	v_lshrrev_b32_e32 v53, 6, v53
	v_lshrrev_b32_e32 v54, 9, v51
	v_add_u32_e32 v53, 0x30e, v53
	v_cndmask_b32_e32 v53, v53, v54, vcc
	v_min_u32_e32 v53, 0x447, v53
	v_lshlrev_b32_e32 v53, 2, v53
	ds_read_b32 v53, v53
	v_cmp_le_i32_e32 vcc, 0, v51
	s_waitcnt lgkmcnt(0)
	v_add_u32_e32 v53, v53, v61
	v_lshlrev_b32_e32 v53, 3, v53
	s_and_b64 exec, s[38:39], vcc
	global_store_dwordx2 v53, v[50:51], s[34:35]
	s_mov_b64 exec, s[38:39]
	v_add_u32_e32 v61, 0xc00, v0
	v_lshlrev_b32_e32 v62, 3, v61
	ds_read_b64 v[50:51], v62 offset:14336
	s_waitcnt lgkmcnt(0)
	v_subrev_co_u32_e32 v53, vcc, 0x61a80, v51
	v_lshrrev_b32_e32 v53, 6, v53
	v_lshrrev_b32_e32 v54, 9, v51
	v_add_u32_e32 v53, 0x30e, v53
	v_cndmask_b32_e32 v53, v53, v54, vcc
	v_min_u32_e32 v53, 0x447, v53
	v_lshlrev_b32_e32 v53, 2, v53
	ds_read_b32 v53, v53
	v_cmp_le_i32_e32 vcc, 0, v51
	s_waitcnt lgkmcnt(0)
	v_add_u32_e32 v53, v53, v61
	v_lshlrev_b32_e32 v53, 3, v53
	s_and_b64 exec, s[38:39], vcc
	global_store_dwordx2 v53, v[50:51], s[34:35]
	s_mov_b64 exec, s[38:39]
	v_add_u32_e32 v61, 0x1000, v0
	v_lshlrev_b32_e32 v62, 3, v61
	ds_read_b64 v[50:51], v62 offset:14336
	s_waitcnt lgkmcnt(0)
	v_subrev_co_u32_e32 v53, vcc, 0x61a80, v51
	v_lshrrev_b32_e32 v53, 6, v53
	v_lshrrev_b32_e32 v54, 9, v51
	v_add_u32_e32 v53, 0x30e, v53
	v_cndmask_b32_e32 v53, v53, v54, vcc
	v_min_u32_e32 v53, 0x447, v53
	v_lshlrev_b32_e32 v53, 2, v53
	ds_read_b32 v53, v53
	v_cmp_le_i32_e32 vcc, 0, v51
	s_waitcnt lgkmcnt(0)
	v_add_u32_e32 v53, v53, v61
	v_lshlrev_b32_e32 v53, 3, v53
	s_and_b64 exec, s[38:39], vcc
	global_store_dwordx2 v53, v[50:51], s[34:35]
	s_mov_b64 exec, s[38:39]
	v_add_u32_e32 v61, 0x1400, v0
	v_lshlrev_b32_e32 v62, 3, v61
	ds_read_b64 v[50:51], v62 offset:14336
	s_waitcnt lgkmcnt(0)
	v_subrev_co_u32_e32 v53, vcc, 0x61a80, v51
	v_lshrrev_b32_e32 v53, 6, v53
	v_lshrrev_b32_e32 v54, 9, v51
	v_add_u32_e32 v53, 0x30e, v53
	v_cndmask_b32_e32 v53, v53, v54, vcc
	v_min_u32_e32 v53, 0x447, v53
	v_lshlrev_b32_e32 v53, 2, v53
	ds_read_b32 v53, v53
	v_cmp_le_i32_e32 vcc, 0, v51
	s_waitcnt lgkmcnt(0)
	v_add_u32_e32 v53, v53, v61
	v_lshlrev_b32_e32 v53, 3, v53
	s_and_b64 exec, s[38:39], vcc
	global_store_dwordx2 v53, v[50:51], s[34:35]
	s_mov_b64 exec, s[38:39]
	v_add_u32_e32 v61, 0x1800, v0
	v_lshlrev_b32_e32 v62, 3, v61
	ds_read_b64 v[50:51], v62 offset:14336
	s_waitcnt lgkmcnt(0)
	v_subrev_co_u32_e32 v53, vcc, 0x61a80, v51
	v_lshrrev_b32_e32 v53, 6, v53
	v_lshrrev_b32_e32 v54, 9, v51
	v_add_u32_e32 v53, 0x30e, v53
	v_cndmask_b32_e32 v53, v53, v54, vcc
	v_min_u32_e32 v53, 0x447, v53
	v_lshlrev_b32_e32 v53, 2, v53
	ds_read_b32 v53, v53
	v_cmp_le_i32_e32 vcc, 0, v51
	s_waitcnt lgkmcnt(0)
	v_add_u32_e32 v53, v53, v61
	v_lshlrev_b32_e32 v53, 3, v53
	s_and_b64 exec, s[38:39], vcc
	global_store_dwordx2 v53, v[50:51], s[34:35]
	s_mov_b64 exec, s[38:39]
	v_add_u32_e32 v61, 0x1c00, v0
	v_lshlrev_b32_e32 v62, 3, v61
	ds_read_b64 v[50:51], v62 offset:14336
	s_waitcnt lgkmcnt(0)
	v_subrev_co_u32_e32 v53, vcc, 0x61a80, v51
	v_lshrrev_b32_e32 v53, 6, v53
	v_lshrrev_b32_e32 v54, 9, v51
	v_add_u32_e32 v53, 0x30e, v53
	v_cndmask_b32_e32 v53, v53, v54, vcc
	v_min_u32_e32 v53, 0x447, v53
	v_lshlrev_b32_e32 v53, 2, v53
	ds_read_b32 v53, v53
	v_cmp_le_i32_e32 vcc, 0, v51
	s_waitcnt lgkmcnt(0)
	v_add_u32_e32 v53, v53, v61
	v_lshlrev_b32_e32 v53, 3, v53
	s_and_b64 exec, s[38:39], vcc
	global_store_dwordx2 v53, v[50:51], s[34:35]
	s_mov_b64 exec, s[38:39]
	s_barrier
	v_subrev_u32_e32 v51, 0x2000, v34
	v_cmp_gt_u32_e32 vcc, s14, v51
	v_lshlrev_b32_e32 v52, 3, v51
	s_and_b64 exec, s[38:39], vcc
	ds_write_b64 v52, v[2:3] offset:14336
	s_mov_b64 exec, s[38:39]
	v_subrev_u32_e32 v51, 0x2000, v35
	v_cmp_gt_u32_e32 vcc, s14, v51
	v_lshlrev_b32_e32 v52, 3, v51
	s_and_b64 exec, s[38:39], vcc
	ds_write_b64 v52, v[4:5] offset:14336
	s_mov_b64 exec, s[38:39]
	v_subrev_u32_e32 v51, 0x2000, v36
	v_cmp_gt_u32_e32 vcc, s14, v51
	v_lshlrev_b32_e32 v52, 3, v51
	s_and_b64 exec, s[38:39], vcc
	ds_write_b64 v52, v[6:7] offset:14336
	s_mov_b64 exec, s[38:39]
	v_subrev_u32_e32 v51, 0x2000, v37
	v_cmp_gt_u32_e32 vcc, s14, v51
	v_lshlrev_b32_e32 v52, 3, v51
	s_and_b64 exec, s[38:39], vcc
	ds_write_b64 v52, v[8:9] offset:14336
	s_mov_b64 exec, s[38:39]
	v_subrev_u32_e32 v51, 0x2000, v38
	v_cmp_gt_u32_e32 vcc, s14, v51
	v_lshlrev_b32_e32 v52, 3, v51
	s_and_b64 exec, s[38:39], vcc
	ds_write_b64 v52, v[10:11] offset:14336
	s_mov_b64 exec, s[38:39]
	v_subrev_u32_e32 v51, 0x2000, v39
	v_cmp_gt_u32_e32 vcc, s14, v51
	v_lshlrev_b32_e32 v52, 3, v51
	s_and_b64 exec, s[38:39], vcc
	ds_write_b64 v52, v[12:13] offset:14336
	s_mov_b64 exec, s[38:39]
	v_subrev_u32_e32 v51, 0x2000, v40
	v_cmp_gt_u32_e32 vcc, s14, v51
	v_lshlrev_b32_e32 v52, 3, v51
	s_and_b64 exec, s[38:39], vcc
	ds_write_b64 v52, v[14:15] offset:14336
	s_mov_b64 exec, s[38:39]
	v_subrev_u32_e32 v51, 0x2000, v41
	v_cmp_gt_u32_e32 vcc, s14, v51
	v_lshlrev_b32_e32 v52, 3, v51
	s_and_b64 exec, s[38:39], vcc
	ds_write_b64 v52, v[16:17] offset:14336
	s_mov_b64 exec, s[38:39]
	v_subrev_u32_e32 v51, 0x2000, v42
	v_cmp_gt_u32_e32 vcc, s14, v51
	v_lshlrev_b32_e32 v52, 3, v51
	s_and_b64 exec, s[38:39], vcc
	ds_write_b64 v52, v[18:19] offset:14336
	s_mov_b64 exec, s[38:39]
	v_subrev_u32_e32 v51, 0x2000, v43
	v_cmp_gt_u32_e32 vcc, s14, v51
	v_lshlrev_b32_e32 v52, 3, v51
	s_and_b64 exec, s[38:39], vcc
	ds_write_b64 v52, v[20:21] offset:14336
	s_mov_b64 exec, s[38:39]
	v_subrev_u32_e32 v51, 0x2000, v44
	v_cmp_gt_u32_e32 vcc, s14, v51
	v_lshlrev_b32_e32 v52, 3, v51
	s_and_b64 exec, s[38:39], vcc
	ds_write_b64 v52, v[22:23] offset:14336
	s_mov_b64 exec, s[38:39]
	v_subrev_u32_e32 v51, 0x2000, v45
	v_cmp_gt_u32_e32 vcc, s14, v51
	v_lshlrev_b32_e32 v52, 3, v51
	s_and_b64 exec, s[38:39], vcc
	ds_write_b64 v52, v[24:25] offset:14336
	s_mov_b64 exec, s[38:39]
	v_subrev_u32_e32 v51, 0x2000, v46
	v_cmp_gt_u32_e32 vcc, s14, v51
	v_lshlrev_b32_e32 v52, 3, v51
	s_and_b64 exec, s[38:39], vcc
	ds_write_b64 v52, v[26:27] offset:14336
	s_mov_b64 exec, s[38:39]
	v_subrev_u32_e32 v51, 0x2000, v47
	v_cmp_gt_u32_e32 vcc, s14, v51
	v_lshlrev_b32_e32 v52, 3, v51
	s_and_b64 exec, s[38:39], vcc
	ds_write_b64 v52, v[28:29] offset:14336
	s_mov_b64 exec, s[38:39]
	v_subrev_u32_e32 v51, 0x2000, v48
	v_cmp_gt_u32_e32 vcc, s14, v51
	v_lshlrev_b32_e32 v52, 3, v51
	s_and_b64 exec, s[38:39], vcc
	ds_write_b64 v52, v[30:31] offset:14336
	s_mov_b64 exec, s[38:39]
	v_subrev_u32_e32 v51, 0x2000, v49
	v_cmp_gt_u32_e32 vcc, s14, v51
	v_lshlrev_b32_e32 v52, 3, v51
	s_and_b64 exec, s[38:39], vcc
	ds_write_b64 v52, v[32:33] offset:14336
	s_mov_b64 exec, s[38:39]
	s_waitcnt lgkmcnt(0)
	s_barrier
	v_mov_b32_e32 v61, v0
	v_lshlrev_b32_e32 v62, 3, v61
	ds_read_b64 v[50:51], v62 offset:14336
	s_waitcnt lgkmcnt(0)
	v_subrev_co_u32_e32 v53, vcc, 0x61a80, v51
	v_lshrrev_b32_e32 v53, 6, v53
	v_lshrrev_b32_e32 v54, 9, v51
	v_add_u32_e32 v53, 0x30e, v53
	v_cndmask_b32_e32 v53, v53, v54, vcc
	v_min_u32_e32 v53, 0x447, v53
	v_lshlrev_b32_e32 v53, 2, v53
	ds_read_b32 v53, v53
	v_cmp_le_i32_e32 vcc, 0, v51
	s_waitcnt lgkmcnt(0)
	v_add_u32_e32 v53, v53, v61
	v_add_u32_e32 v53, 0x2000, v53
	v_lshlrev_b32_e32 v53, 3, v53
	s_and_b64 exec, s[38:39], vcc
	global_store_dwordx2 v53, v[50:51], s[34:35]
	s_mov_b64 exec, s[38:39]
	v_add_u32_e32 v61, 0x400, v0
	v_lshlrev_b32_e32 v62, 3, v61
	ds_read_b64 v[50:51], v62 offset:14336
	s_waitcnt lgkmcnt(0)
	v_subrev_co_u32_e32 v53, vcc, 0x61a80, v51
	v_lshrrev_b32_e32 v53, 6, v53
	v_lshrrev_b32_e32 v54, 9, v51
	v_add_u32_e32 v53, 0x30e, v53
	v_cndmask_b32_e32 v53, v53, v54, vcc
	v_min_u32_e32 v53, 0x447, v53
	v_lshlrev_b32_e32 v53, 2, v53
	ds_read_b32 v53, v53
	v_cmp_le_i32_e32 vcc, 0, v51
	s_waitcnt lgkmcnt(0)
	v_add_u32_e32 v53, v53, v61
	v_add_u32_e32 v53, 0x2000, v53
	v_lshlrev_b32_e32 v53, 3, v53
	s_and_b64 exec, s[38:39], vcc
	global_store_dwordx2 v53, v[50:51], s[34:35]
	s_mov_b64 exec, s[38:39]
	v_add_u32_e32 v61, 0x800, v0
	v_lshlrev_b32_e32 v62, 3, v61
	ds_read_b64 v[50:51], v62 offset:14336
	s_waitcnt lgkmcnt(0)
	v_subrev_co_u32_e32 v53, vcc, 0x61a80, v51
	v_lshrrev_b32_e32 v53, 6, v53
	v_lshrrev_b32_e32 v54, 9, v51
	v_add_u32_e32 v53, 0x30e, v53
	v_cndmask_b32_e32 v53, v53, v54, vcc
	v_min_u32_e32 v53, 0x447, v53
	v_lshlrev_b32_e32 v53, 2, v53
	ds_read_b32 v53, v53
	v_cmp_le_i32_e32 vcc, 0, v51
	s_waitcnt lgkmcnt(0)
	v_add_u32_e32 v53, v53, v61
	v_add_u32_e32 v53, 0x2000, v53
	v_lshlrev_b32_e32 v53, 3, v53
	s_and_b64 exec, s[38:39], vcc
	global_store_dwordx2 v53, v[50:51], s[34:35]
	s_mov_b64 exec, s[38:39]
	v_add_u32_e32 v61, 0xc00, v0
	v_lshlrev_b32_e32 v62, 3, v61
	ds_read_b64 v[50:51], v62 offset:14336
	s_waitcnt lgkmcnt(0)
	v_subrev_co_u32_e32 v53, vcc, 0x61a80, v51
	v_lshrrev_b32_e32 v53, 6, v53
	v_lshrrev_b32_e32 v54, 9, v51
	v_add_u32_e32 v53, 0x30e, v53
	v_cndmask_b32_e32 v53, v53, v54, vcc
	v_min_u32_e32 v53, 0x447, v53
	v_lshlrev_b32_e32 v53, 2, v53
	ds_read_b32 v53, v53
	v_cmp_le_i32_e32 vcc, 0, v51
	s_waitcnt lgkmcnt(0)
	v_add_u32_e32 v53, v53, v61
	v_add_u32_e32 v53, 0x2000, v53
	v_lshlrev_b32_e32 v53, 3, v53
	s_and_b64 exec, s[38:39], vcc
	global_store_dwordx2 v53, v[50:51], s[34:35]
	s_mov_b64 exec, s[38:39]
	v_add_u32_e32 v61, 0x1000, v0
	v_lshlrev_b32_e32 v62, 3, v61
	ds_read_b64 v[50:51], v62 offset:14336
	s_waitcnt lgkmcnt(0)
	v_subrev_co_u32_e32 v53, vcc, 0x61a80, v51
	v_lshrrev_b32_e32 v53, 6, v53
	v_lshrrev_b32_e32 v54, 9, v51
	v_add_u32_e32 v53, 0x30e, v53
	v_cndmask_b32_e32 v53, v53, v54, vcc
	v_min_u32_e32 v53, 0x447, v53
	v_lshlrev_b32_e32 v53, 2, v53
	ds_read_b32 v53, v53
	v_cmp_le_i32_e32 vcc, 0, v51
	s_waitcnt lgkmcnt(0)
	v_add_u32_e32 v53, v53, v61
	v_add_u32_e32 v53, 0x2000, v53
	v_lshlrev_b32_e32 v53, 3, v53
	s_and_b64 exec, s[38:39], vcc
	global_store_dwordx2 v53, v[50:51], s[34:35]
	s_mov_b64 exec, s[38:39]
	v_add_u32_e32 v61, 0x1400, v0
	v_lshlrev_b32_e32 v62, 3, v61
	ds_read_b64 v[50:51], v62 offset:14336
	s_waitcnt lgkmcnt(0)
	v_subrev_co_u32_e32 v53, vcc, 0x61a80, v51
	v_lshrrev_b32_e32 v53, 6, v53
	v_lshrrev_b32_e32 v54, 9, v51
	v_add_u32_e32 v53, 0x30e, v53
	v_cndmask_b32_e32 v53, v53, v54, vcc
	v_min_u32_e32 v53, 0x447, v53
	v_lshlrev_b32_e32 v53, 2, v53
	ds_read_b32 v53, v53
	v_cmp_le_i32_e32 vcc, 0, v51
	s_waitcnt lgkmcnt(0)
	v_add_u32_e32 v53, v53, v61
	v_add_u32_e32 v53, 0x2000, v53
	v_lshlrev_b32_e32 v53, 3, v53
	s_and_b64 exec, s[38:39], vcc
	global_store_dwordx2 v53, v[50:51], s[34:35]
	s_mov_b64 exec, s[38:39]
	v_add_u32_e32 v61, 0x1800, v0
	v_lshlrev_b32_e32 v62, 3, v61
	ds_read_b64 v[50:51], v62 offset:14336
	s_waitcnt lgkmcnt(0)
	v_subrev_co_u32_e32 v53, vcc, 0x61a80, v51
	v_lshrrev_b32_e32 v53, 6, v53
	v_lshrrev_b32_e32 v54, 9, v51
	v_add_u32_e32 v53, 0x30e, v53
	v_cndmask_b32_e32 v53, v53, v54, vcc
	v_min_u32_e32 v53, 0x447, v53
	v_lshlrev_b32_e32 v53, 2, v53
	ds_read_b32 v53, v53
	v_cmp_le_i32_e32 vcc, 0, v51
	s_waitcnt lgkmcnt(0)
	v_add_u32_e32 v53, v53, v61
	v_add_u32_e32 v53, 0x2000, v53
	v_lshlrev_b32_e32 v53, 3, v53
	s_and_b64 exec, s[38:39], vcc
	global_store_dwordx2 v53, v[50:51], s[34:35]
	s_mov_b64 exec, s[38:39]
	v_add_u32_e32 v61, 0x1c00, v0
	v_lshlrev_b32_e32 v62, 3, v61
	ds_read_b64 v[50:51], v62 offset:14336
	s_waitcnt lgkmcnt(0)
	v_subrev_co_u32_e32 v53, vcc, 0x61a80, v51
	v_lshrrev_b32_e32 v53, 6, v53
	v_lshrrev_b32_e32 v54, 9, v51
	v_add_u32_e32 v53, 0x30e, v53
	v_cndmask_b32_e32 v53, v53, v54, vcc
	v_min_u32_e32 v53, 0x447, v53
	v_lshlrev_b32_e32 v53, 2, v53
	ds_read_b32 v53, v53
	v_cmp_le_i32_e32 vcc, 0, v51
	s_waitcnt lgkmcnt(0)
	v_add_u32_e32 v53, v53, v61
	v_add_u32_e32 v53, 0x2000, v53
	v_lshlrev_b32_e32 v53, 3, v53
	s_and_b64 exec, s[38:39], vcc
	global_store_dwordx2 v53, v[50:51], s[34:35]
	s_mov_b64 exec, s[38:39]
	s_endpgm

	.amdhsa_kernel _Z6k_prepPKiS0_S0_S0_PiP15HIP_vector_typeIiLj2EEPKfS6_S0_S0_S0_S6_S6_S6_PDF16_S7_6WSpecs
		.amdhsa_group_segment_fixed_size 79872
		.amdhsa_private_segment_fixed_size 0
		.amdhsa_kernarg_size 616
		.amdhsa_user_sgpr_count 2
		.amdhsa_user_sgpr_dispatch_ptr 0
		.amdhsa_user_sgpr_queue_ptr 0
		.amdhsa_user_sgpr_kernarg_segment_ptr 1
		.amdhsa_user_sgpr_dispatch_id 0
		.amdhsa_user_sgpr_kernarg_preload_length 0
		.amdhsa_user_sgpr_kernarg_preload_offset 0
		.amdhsa_user_sgpr_private_segment_size 0
		.amdhsa_uses_dynamic_stack 0
		.amdhsa_enable_private_segment 0
		.amdhsa_system_sgpr_workgroup_id_x 1
		.amdhsa_system_sgpr_workgroup_id_y 0
		.amdhsa_system_sgpr_workgroup_id_z 0
		.amdhsa_system_sgpr_workgroup_info 0
		.amdhsa_system_vgpr_workitem_id 0
		.amdhsa_next_free_vgpr 128
		.amdhsa_next_free_sgpr 40
		.amdhsa_accum_offset 128
		.amdhsa_reserve_vcc 1
		.amdhsa_float_round_mode_32 0
		.amdhsa_float_round_mode_16_64 0
		.amdhsa_float_denorm_mode_32 3
		.amdhsa_float_denorm_mode_16_64 3
		.amdhsa_dx10_clamp 1
		.amdhsa_ieee_mode 1
		.amdhsa_fp16_overflow 0
		.amdhsa_tg_split 0
		.amdhsa_exception_fp_ieee_invalid_op 0
		.amdhsa_exception_fp_denorm_src 0
		.amdhsa_exception_fp_ieee_div_zero 0
		.amdhsa_exception_fp_ieee_overflow 0
		.amdhsa_exception_fp_ieee_underflow 0
		.amdhsa_exception_fp_ieee_inexact 0
		.amdhsa_exception_int_div_zero 0
	.end_amdhsa_kernel

amdhsa.kernels:
  - .agpr_count:     0
    .args:
      - .actual_access:  read_only
        .address_space:  global
        .offset:         0
        .size:           8
        .value_kind:     global_buffer
      - .actual_access:  read_only
        .address_space:  global
        .offset:         8
        .size:           8
        .value_kind:     global_buffer
      - .actual_access:  write_only
        .address_space:  global
        .offset:         16
        .size:           8
        .value_kind:     global_buffer
      - .address_space:  global
        .offset:         24
        .size:           8
        .value_kind:     global_buffer
    .group_segment_fixed_size: 20736
    .kernarg_segment_align: 8
    .kernarg_segment_size: 32
    .language:       OpenCL C
    .language_version:
      - 2
      - 0
    .max_flat_workgroup_size: 256
    .name:           _Z6k_bcsrPK15HIP_vector_typeIiLj2EEPKiPiS5_
    .private_segment_fixed_size: 0
    .sgpr_count:     40
    .sgpr_spill_count: 0
    .symbol:         _Z6k_bcsrPK15HIP_vector_typeIiLj2EEPKiPiS5_.kd
    .uniform_work_group_size: 1
    .uses_dynamic_stack: false
    .vgpr_count:     64
    .vgpr_spill_count: 0
    .wavefront_size: 64
  - .agpr_count:     0
    .args:
      - .actual_access:  read_only
        .address_space:  global
        .offset:         0
        .size:           8
        .value_kind:     global_buffer
      - .actual_access:  read_only
        .address_space:  global
        .offset:         8
        .size:           8
        .value_kind:     global_buffer
      - .actual_access:  read_only
        .address_space:  global
        .offset:         16
        .size:           8
        .value_kind:     global_buffer
      - .actual_access:  write_only
        .address_space:  global
        .offset:         24
        .size:           8
        .value_kind:     global_buffer
      - .actual_access:  write_only
        .address_space:  global
        .offset:         32
        .size:           8
        .value_kind:     global_buffer
      - .actual_access:  read_only
        .address_space:  global
        .offset:         40
        .size:           8
        .value_kind:     global_buffer
      - .actual_access:  read_only
        .address_space:  global
        .offset:         48
        .size:           8
        .value_kind:     global_buffer
      - .actual_access:  read_only
        .address_space:  global
        .offset:         56
        .size:           8
        .value_kind:     global_buffer
      - .actual_access:  read_only
        .address_space:  global
        .offset:         64
        .size:           8
        .value_kind:     global_buffer
      - .actual_access:  read_only
        .address_space:  global
        .offset:         72
        .size:           8
        .value_kind:     global_buffer
      - .actual_access:  read_only
        .address_space:  global
        .offset:         80
        .size:           8
        .value_kind:     global_buffer
      - .actual_access:  read_only
        .address_space:  global
        .offset:         88
        .size:           8
        .value_kind:     global_buffer
      - .actual_access:  read_only
        .address_space:  global
        .offset:         96
        .size:           8
        .value_kind:     global_buffer
      - .address_space:  global
        .offset:         104
        .size:           8
        .value_kind:     global_buffer
      - .address_space:  global
        .offset:         112
        .size:           8
        .value_kind:     global_buffer
    .group_segment_fixed_size: 4384
    .kernarg_segment_align: 8
    .kernarg_segment_size: 120
    .language:       OpenCL C
    .language_version:
      - 2
      - 0
    .max_flat_workgroup_size: 1024
    .name:           _Z8k_bcountPKiS0_S0_PiPjPKfS4_S0_S0_S0_S4_S4_S4_PDF16_S5_
    .private_segment_fixed_size: 0
    .sgpr_count:     26
    .sgpr_spill_count: 0
    .symbol:         _Z8k_bcountPKiS0_S0_PiPjPKfS4_S0_S0_S0_S4_S4_S4_PDF16_S5_.kd
    .uniform_work_group_size: 1
    .uses_dynamic_stack: false
    .vgpr_count:     41
    .vgpr_spill_count: 0
    .wavefront_size: 64
  - .agpr_count:     0
    .args:
      - .actual_access:  read_only
        .address_space:  global
        .offset:         0
        .size:           8
        .value_kind:     global_buffer
      - .actual_access:  read_only
        .address_space:  global
        .offset:         8
        .size:           8
        .value_kind:     global_buffer
      - .actual_access:  read_only
        .address_space:  global
        .offset:         16
        .size:           8
        .value_kind:     global_buffer
      - .actual_access:  read_only
        .address_space:  global
        .offset:         24
        .size:           8
        .value_kind:     global_buffer
      - .actual_access:  write_only
        .address_space:  global
        .offset:         32
        .size:           8
        .value_kind:     global_buffer
      - .actual_access:  write_only
        .address_space:  global
        .offset:         40
        .size:           8
        .value_kind:     global_buffer
      - .actual_access:  read_only
        .address_space:  global
        .offset:         48
        .size:           8
        .value_kind:     global_buffer
      - .actual_access:  read_only
        .address_space:  global
        .offset:         56
        .size:           8
        .value_kind:     global_buffer
      - .actual_access:  read_only
        .address_space:  global
        .offset:         64
        .size:           8
        .value_kind:     global_buffer
      - .actual_access:  read_only
        .address_space:  global
        .offset:         72
        .size:           8
        .value_kind:     global_buffer
      - .actual_access:  read_only
        .address_space:  global
        .offset:         80
        .size:           8
        .value_kind:     global_buffer
      - .actual_access:  read_only
        .address_space:  global
        .offset:         88
        .size:           8
        .value_kind:     global_buffer
      - .actual_access:  read_only
        .address_space:  global
        .offset:         96
        .size:           8
        .value_kind:     global_buffer
      - .actual_access:  read_only
        .address_space:  global
        .offset:         104
        .size:           8
        .value_kind:     global_buffer
      - .address_space:  global
        .offset:         112
        .size:           8
        .value_kind:     global_buffer
      - .address_space:  global
        .offset:         120
        .size:           8
        .value_kind:     global_buffer
      - .offset:         128
        .size:           488
        .value_kind:     by_value
    .group_segment_fixed_size: 79872
    .kernarg_segment_align: 8
    .kernarg_segment_size: 616
    .language:       OpenCL C
    .language_version:
      - 2
      - 0
    .max_flat_workgroup_size: 1024
    .name:           _Z6k_prepPKiS0_S0_S0_PiP15HIP_vector_typeIiLj2EEPKfS6_S0_S0_S0_S6_S6_S6_PDF16_S7_6WSpecs
    .private_segment_fixed_size: 0
    .sgpr_count:     44
    .sgpr_spill_count: 0
    .symbol:         _Z6k_prepPKiS0_S0_S0_PiP15HIP_vector_typeIiLj2EEPKfS6_S0_S0_S0_S6_S6_S6_PDF16_S7_6WSpecs.kd
    .uniform_work_group_size: 1
    .uses_dynamic_stack: false
    .vgpr_count:     128
    .vgpr_spill_count: 0
    .wavefront_size: 64
  - .agpr_count:     0
    .args:
      - .offset:         0
        .size:           104
        .value_kind:     by_value
      - .offset:         104
        .size:           4
        .value_kind:     hidden_block_count_x
      - .offset:         108
        .size:           4
        .value_kind:     hidden_block_count_y
      - .offset:         112
        .size:           4
        .value_kind:     hidden_block_count_z
      - .offset:         116
        .size:           2
        .value_kind:     hidden_group_size_x
      - .offset:         118
        .size:           2
        .value_kind:     hidden_group_size_y
      - .offset:         120
        .size:           2
        .value_kind:     hidden_group_size_z
      - .offset:         122
        .size:           2
        .value_kind:     hidden_remainder_x
      - .offset:         124
        .size:           2
        .value_kind:     hidden_remainder_y
      - .offset:         126
        .size:           2
        .value_kind:     hidden_remainder_z
      - .offset:         144
        .size:           8
        .value_kind:     hidden_global_offset_x
      - .offset:         152
        .size:           8
        .value_kind:     hidden_global_offset_y
      - .offset:         160
        .size:           8
        .value_kind:     hidden_global_offset_z
      - .offset:         168
        .size:           2
        .value_kind:     hidden_grid_dims
    .group_segment_fixed_size: 155140
    .kernarg_segment_align: 8
    .kernarg_segment_size: 360
    .language:       OpenCL C
    .language_version:
      - 2
      - 0
    .max_flat_workgroup_size: 768
    .name:           _Z12k_layer_pool9LayerArgs
    .private_segment_fixed_size: 0
    .sgpr_count:     50
    .sgpr_spill_count: 0
    .symbol:         _Z12k_layer_pool9LayerArgs.kd
    .uniform_work_group_size: 1
    .uses_dynamic_stack: false
    .vgpr_count:     168
    .vgpr_spill_count: 0
    .wavefront_size: 64
  - .agpr_count:     0
    .args:
      - .actual_access:  read_only
        .address_space:  global
        .offset:         0
        .size:           8
        .value_kind:     global_buffer
      - .actual_access:  read_only
        .address_space:  global
        .offset:         8
        .size:           8
        .value_kind:     global_buffer
      - .actual_access:  read_only
        .address_space:  global
        .offset:         16
        .size:           8
        .value_kind:     global_buffer
      - .actual_access:  read_only
        .address_space:  global
        .offset:         24
        .size:           8
        .value_kind:     global_buffer
      - .actual_access:  read_only
        .address_space:  global
        .offset:         32
        .size:           8
        .value_kind:     global_buffer
      - .actual_access:  read_only
        .address_space:  global
        .offset:         40
        .size:           8
        .value_kind:     global_buffer
      - .actual_access:  read_only
        .address_space:  global
        .offset:         48
        .size:           8
        .value_kind:     global_buffer
      - .actual_access:  write_only
        .address_space:  global
        .offset:         56
        .size:           8
        .value_kind:     global_buffer
    .group_segment_fixed_size: 2560
    .kernarg_segment_align: 8
    .kernarg_segment_size: 64
    .language:       OpenCL C
    .language_version:
      - 2
      - 0
    .max_flat_workgroup_size: 512
    .name:           _Z5k_mlpPKjPKfS2_S2_S2_S2_S2_Pf
    .private_segment_fixed_size: 0
    .sgpr_count:     18
    .sgpr_spill_count: 0
    .symbol:         _Z5k_mlpPKjPKfS2_S2_S2_S2_S2_Pf.kd
    .uniform_work_group_size: 1
    .uses_dynamic_stack: false
    .vgpr_count:     120
    .vgpr_spill_count: 0
    .wavefront_size: 64
  - .agpr_count:     0
    .args:
      - .offset:         0
        .size:           104
        .value_kind:     by_value
      - .offset:         104
        .size:           104
        .value_kind:     by_value
      - .offset:         208
        .size:           4
        .value_kind:     by_value
      - .offset:         216
        .size:           4
        .value_kind:     hidden_block_count_x
      - .offset:         220
        .size:           4
        .value_kind:     hidden_block_count_y
      - .offset:         224
        .size:           4
        .value_kind:     hidden_block_count_z
      - .offset:         228
        .size:           2
        .value_kind:     hidden_group_size_x
      - .offset:         230
        .size:           2
        .value_kind:     hidden_group_size_y
      - .offset:         232
        .size:           2
        .value_kind:     hidden_group_size_z
      - .offset:         234
        .size:           2
        .value_kind:     hidden_remainder_x
      - .offset:         236
        .size:           2
        .value_kind:     hidden_remainder_y
      - .offset:         238
        .size:           2
        .value_kind:     hidden_remainder_z
      - .offset:         256
        .size:           8
        .value_kind:     hidden_global_offset_x
      - .offset:         264
        .size:           8
        .value_kind:     hidden_global_offset_y
      - .offset:         272
        .size:           8
        .value_kind:     hidden_global_offset_z
      - .offset:         280
        .size:           2
        .value_kind:     hidden_grid_dims
    .group_segment_fixed_size: 151044
    .kernarg_segment_align: 8
    .kernarg_segment_size: 472
    .language:       OpenCL C
    .language_version:
      - 2
      - 0
    .max_flat_workgroup_size: 768
    .name:           _Z10k_layer_fhILi96ELb1EEv9LayerArgsS0_i
    .private_segment_fixed_size: 0
    .sgpr_count:     52
    .sgpr_spill_count: 0
    .symbol:         _Z10k_layer_fhILi96ELb1EEv9LayerArgsS0_i.kd
    .uniform_work_group_size: 1
    .uses_dynamic_stack: false
    .vgpr_count:     168
    .vgpr_spill_count: 0
    .wavefront_size: 64
  - .agpr_count:     0
    .args:
      - .offset:         0
        .size:           104
        .value_kind:     by_value
      - .offset:         104
        .size:           104
        .value_kind:     by_value
      - .offset:         208
        .size:           4
        .value_kind:     by_value
      - .offset:         216
        .size:           4
        .value_kind:     hidden_block_count_x
      - .offset:         220
        .size:           4
        .value_kind:     hidden_block_count_y
      - .offset:         224
        .size:           4
        .value_kind:     hidden_block_count_z
      - .offset:         228
        .size:           2
        .value_kind:     hidden_group_size_x
      - .offset:         230
        .size:           2
        .value_kind:     hidden_group_size_y
      - .offset:         232
        .size:           2
        .value_kind:     hidden_group_size_z
      - .offset:         234
        .size:           2
        .value_kind:     hidden_remainder_x
      - .offset:         236
        .size:           2
        .value_kind:     hidden_remainder_y
      - .offset:         238
        .size:           2
        .value_kind:     hidden_remainder_z
      - .offset:         256
        .size:           8
        .value_kind:     hidden_global_offset_x
      - .offset:         264
        .size:           8
        .value_kind:     hidden_global_offset_y
      - .offset:         272
        .size:           8
        .value_kind:     hidden_global_offset_z
      - .offset:         280
        .size:           2
        .value_kind:     hidden_grid_dims
    .group_segment_fixed_size: 151044
    .kernarg_segment_align: 8
    .kernarg_segment_size: 472
    .language:       OpenCL C
    .language_version:
      - 2
      - 0
    .max_flat_workgroup_size: 768
    .name:           _Z10k_layer_fhILi128ELb1EEv9LayerArgsS0_i
    .private_segment_fixed_size: 0
    .sgpr_count:     45
    .sgpr_spill_count: 0
    .symbol:         _Z10k_layer_fhILi128ELb1EEv9LayerArgsS0_i.kd
    .uniform_work_group_size: 1
    .uses_dynamic_stack: false
    .vgpr_count:     168
    .vgpr_spill_count: 0
    .wavefront_size: 64
